# router phase: LDS weight reads of the row dot products kept 7 in flight through a ring of 8 register quads (was 2 with a wait before almost every use); same arithmetic and order
# speedup vs baseline: 1.0095x; 1.0078x over previous
.LBB0_1376:
	v_mov_b32_e32 v78, v43
	v_mov_b32_e32 v79, v45
	v_mov_b32_e32 v76, v42
	v_mov_b32_e32 v77, v44
	v_pk_mul_f32 v[78:79], v[78:79], v[78:79]
	v_mov_b32_e32 v80, v47
	v_mov_b32_e32 v81, v51
	v_pk_fma_f32 v[76:77], v[76:77], v[76:77], v[78:79]
	v_mov_b32_e32 v78, v46
	v_mov_b32_e32 v79, v50
	v_pk_mul_f32 v[80:81], v[80:81], v[80:81]
	v_lshl_add_u64 v[74:75], s[56:57], 0, v[38:39]
	v_pk_fma_f32 v[78:79], v[78:79], v[78:79], v[80:81]
	v_pk_mul_f32 v[80:81], v[48:49], v[48:49]
	v_pk_add_f32 v[76:77], v[76:77], v[78:79]
	v_pk_mul_f32 v[78:79], v[54:55], v[54:55]
	v_pk_add_f32 v[76:77], v[76:77], v[76:77] op_sel:[0,1] op_sel_hi:[1,0]
	v_pk_mov_b32 v[82:83], v[80:81], v[78:79] op_sel:[1,0]
	v_mov_b32_e32 v81, v79
	v_pk_add_f32 v[78:79], v[82:83], v[80:81]
	v_mul_f32_e32 v80, v56, v56
	v_mul_f32_e32 v81, v57, v57
	v_pk_add_f32 v[78:79], v[78:79], v[78:79] op_sel:[0,1] op_sel_hi:[1,0]
	v_mov_b32_e32 v77, v80
	v_mov_b32_e32 v79, v81
	v_pk_add_f32 v[76:77], v[76:77], v[78:79]
	v_mul_f32_e32 v78, v53, v53
	v_mul_f32_e32 v80, v59, v59
	v_mul_f32_e32 v82, v62, v62
	v_mul_f32_e32 v83, v63, v63
	v_pk_fma_f32 v[78:79], v[52:53], v[52:53], v[78:79] op_sel_hi:[1,1,0]
	v_pk_fma_f32 v[80:81], v[58:59], v[58:59], v[80:81] op_sel_hi:[1,1,0]
	v_mov_b32_e32 v79, v82
	v_mov_b32_e32 v81, v83
	v_pk_add_f32 v[78:79], v[78:79], v[80:81]
	v_pk_mul_f32 v[80:81], v[60:61], v[60:61]
	v_pk_add_f32 v[76:77], v[76:77], v[78:79]
	v_pk_mul_f32 v[78:79], v[66:67], v[66:67]
	v_pk_add_f32 v[76:77], v[76:77], v[76:77] op_sel:[0,1] op_sel_hi:[1,0]
	v_pk_mov_b32 v[82:83], v[80:81], v[78:79] op_sel:[1,0]
	v_mov_b32_e32 v81, v79
	v_pk_add_f32 v[78:79], v[82:83], v[80:81]
	v_mul_f32_e32 v80, v68, v68
	v_mul_f32_e32 v81, v69, v69
	v_pk_add_f32 v[78:79], v[78:79], v[78:79] op_sel:[0,1] op_sel_hi:[1,0]
	v_mov_b32_e32 v77, v80
	v_mov_b32_e32 v79, v81
	v_pk_add_f32 v[76:77], v[76:77], v[78:79]
	v_mul_f32_e32 v78, v65, v65
	v_mul_f32_e32 v80, v71, v71
	v_mul_f32_e32 v82, v72, v72
	v_mul_f32_e32 v83, v73, v73
	v_pk_fma_f32 v[78:79], v[64:65], v[64:65], v[78:79] op_sel_hi:[1,1,0]
	v_pk_fma_f32 v[80:81], v[70:71], v[70:71], v[80:81] op_sel_hi:[1,1,0]
	v_mov_b32_e32 v79, v82
	v_mov_b32_e32 v81, v83
	v_pk_add_f32 v[78:79], v[78:79], v[80:81]
	v_add_co_u32_e32 v74, vcc, s11, v74
	v_pk_add_f32 v[76:77], v[76:77], v[78:79]
	s_nop 0
	v_addc_co_u32_e32 v75, vcc, 0, v75, vcc
	v_add_f32_e32 v76, v76, v77
	global_load_dwordx2 v[90:91], v[74:75], off
	global_load_dwordx2 v[88:89], v[74:75], off offset:512
	global_load_dwordx2 v[82:83], v[74:75], off offset:1024
	global_load_dwordx2 v[80:81], v[74:75], off offset:1536
	v_add_f32_dpp v76, v76, v76 quad_perm:[1,0,3,2] row_mask:0xf bank_mask:0xf bound_ctrl:1
	v_mov_b32_e32 v96, 0
	v_mov_b32_e32 v97, 0
	v_add_f32_dpp v76, v76, v76 quad_perm:[2,3,0,1] row_mask:0xf bank_mask:0xf bound_ctrl:1
	v_mov_b32_e32 v98, 0
	s_nop 0
	v_add_f32_dpp v76, v76, v76 row_half_mirror row_mask:0xf bank_mask:0xf bound_ctrl:1
	s_nop 1
	v_add_f32_dpp v76, v76, v76 row_mirror row_mask:0xf bank_mask:0xf bound_ctrl:1
	s_nop 0
	v_readlane_b32 s6, v76, 16
	v_readlane_b32 s7, v76, 48
	v_readlane_b32 s0, v76, 0
	v_readlane_b32 s1, v76, 32
	v_mov_b32_e32 v76, s6
	v_mov_b32_e32 v77, s7
	v_pk_add_f32 v[76:77], s[0:1], v[76:77]
	s_nop 0
	v_add_f32_e32 v76, v76, v77
	v_fmamk_f32 v76, v76, 0x3a000000, v111
	v_mul_f32_e32 v77, 0x4f800000, v76
	v_cmp_gt_f32_e32 vcc, s35, v76
	s_nop 1
	v_cndmask_b32_e32 v76, v76, v77, vcc
	v_sqrt_f32_e32 v77, v76
	s_nop 0
	v_add_u32_e32 v78, -1, v77
	v_fma_f32 v79, -v78, v77, v76
	v_cmp_ge_f32_e64 s[0:1], 0, v79
	v_add_u32_e32 v79, 1, v77
	s_nop 0
	v_cndmask_b32_e64 v78, v77, v78, s[0:1]
	v_fma_f32 v77, -v79, v77, v76
	v_cmp_lt_f32_e64 s[0:1], 0, v77
	s_nop 1
	v_cndmask_b32_e64 v77, v78, v79, s[0:1]
	v_mul_f32_e32 v78, 0x37800000, v77
	v_cndmask_b32_e32 v77, v77, v78, vcc
	v_cmp_class_f32_e32 vcc, v76, v112
	s_nop 1
	v_cndmask_b32_e32 v92, v77, v76, vcc
	v_div_scale_f32 v93, s[0:1], v92, v92, 1.0
	v_rcp_f32_e32 v94, v93
	global_load_dwordx2 v[86:87], v[74:75], off offset:2048
	global_load_dwordx2 v[84:85], v[74:75], off offset:2560
	global_load_dwordx2 v[78:79], v[74:75], off offset:3072
	global_load_dwordx2 v[76:77], v[74:75], off offset:3584
	v_fma_f32 v74, -v93, v94, 1.0
	v_fmac_f32_e32 v94, v74, v94
	v_div_scale_f32 v74, vcc, 1.0, v92, 1.0
	v_mul_f32_e32 v75, v74, v94
	v_fma_f32 v95, -v93, v75, v74
	v_fmac_f32_e32 v75, v95, v94
	v_fma_f32 v74, -v93, v75, v74
	v_div_fmas_f32 v74, v74, v94, v75
	v_div_fixup_f32 v92, v74, v92, 1.0
	v_pk_mul_f32 v[42:43], v[92:93], v[42:43] op_sel_hi:[0,1]
	s_waitcnt vmcnt(12)
	v_pk_mul_f32 v[42:43], v[42:43], v[14:15]
	v_pk_mul_f32 v[46:47], v[92:93], v[46:47] op_sel_hi:[0,1]
	v_med3_f32 v93, v42, s60, v115
	v_med3_f32 v94, v43, s60, v115
	v_mov_b32_e32 v95, 0
	v_cvt_pk_fp8_f32 v95, v93, v94
	v_pk_mul_f32 v[46:47], v[46:47], v[16:17]
	v_lshl_add_u64 v[74:75], s[56:57], 0, v[40:41]
	v_med3_f32 v93, v46, s60, v115
	v_med3_f32 v94, v47, s60, v115
	v_cvt_pk_fp8_f32 v95, v93, v94 op_sel:[0,0,1]
	v_add_co_u32_e32 v74, vcc, s61, v74
	v_pk_mul_f32 v[44:45], v[92:93], v[44:45] op_sel_hi:[0,1]
	s_nop 0
	v_addc_co_u32_e32 v75, vcc, 0, v75, vcc
	v_pk_mul_f32 v[44:45], v[44:45], v[2:3]
	global_store_dword v[74:75], v95, off
	v_pk_mul_f32 v[50:51], v[92:93], v[50:51] op_sel_hi:[0,1]
	v_med3_f32 v93, v44, s60, v115
	v_med3_f32 v94, v45, s60, v115
	v_mov_b32_e32 v95, 0
	v_cvt_pk_fp8_f32 v95, v93, v94
	v_pk_mul_f32 v[50:51], v[50:51], v[4:5]
	s_nop 0
	v_med3_f32 v93, v50, s60, v115
	v_pk_mul_f32 v[48:49], v[92:93], v[48:49] op_sel_hi:[0,1]
	v_med3_f32 v94, v51, s60, v115
	v_pk_mul_f32 v[48:49], v[48:49], v[6:7]
	v_cvt_pk_fp8_f32 v95, v93, v94 op_sel:[0,0,1]
	v_pk_mul_f32 v[54:55], v[92:93], v[54:55] op_sel_hi:[0,1]
	v_med3_f32 v93, v48, s60, v115
	v_med3_f32 v94, v49, s60, v115
	v_cvt_pk_fp8_f32 v96, v93, v94
	v_pk_mul_f32 v[54:55], v[54:55], v[8:9]
	s_nop 0
	v_med3_f32 v93, v54, s60, v115
	v_pk_mul_f32 v[52:53], v[92:93], v[52:53] op_sel_hi:[0,1]
	v_med3_f32 v94, v55, s60, v115
	v_pk_mul_f32 v[52:53], v[52:53], v[10:11]
	v_cvt_pk_fp8_f32 v96, v93, v94 op_sel:[0,0,1]
	v_pk_mul_f32 v[58:59], v[92:93], v[58:59] op_sel_hi:[0,1]
	v_med3_f32 v93, v52, s60, v115
	v_med3_f32 v94, v53, s60, v115
	v_cvt_pk_fp8_f32 v97, v93, v94
	v_pk_mul_f32 v[58:59], v[58:59], v[12:13]
	s_nop 0
	v_med3_f32 v93, v58, s60, v115
	v_pk_mul_f32 v[56:57], v[92:93], v[56:57] op_sel_hi:[0,1]
	v_med3_f32 v94, v59, s60, v115
	s_waitcnt vmcnt(12)
	v_pk_mul_f32 v[56:57], v[56:57], v[18:19]
	v_cvt_pk_fp8_f32 v97, v93, v94 op_sel:[0,0,1]
	v_pk_mul_f32 v[62:63], v[92:93], v[62:63] op_sel_hi:[0,1]
	v_med3_f32 v93, v56, s60, v115
	v_med3_f32 v94, v57, s60, v115
	v_cvt_pk_fp8_f32 v98, v93, v94
	v_pk_mul_f32 v[62:63], v[62:63], v[20:21]
	s_nop 0
	v_med3_f32 v93, v62, s60, v115
	v_med3_f32 v94, v63, s60, v115
	v_pk_mul_f32 v[60:61], v[92:93], v[60:61] op_sel_hi:[0,1]
	v_cvt_pk_fp8_f32 v98, v93, v94 op_sel:[0,0,1]
	s_waitcnt vmcnt(11)
	v_pk_mul_f32 v[60:61], v[60:61], v[22:23]
	global_store_dword v[74:75], v95, off offset:256
	global_store_dword v[74:75], v96, off offset:512
	global_store_dword v[74:75], v97, off offset:768
	global_store_dword v[74:75], v98, off offset:1024
	v_pk_mul_f32 v[66:67], v[92:93], v[66:67] op_sel_hi:[0,1]
	v_med3_f32 v93, v60, s60, v115
	v_med3_f32 v94, v61, s60, v115
	v_mov_b32_e32 v96, 0
	v_cvt_pk_fp8_f32 v96, v93, v94
	v_pk_mul_f32 v[66:67], v[66:67], v[24:25]
	v_mov_b32_e32 v97, 0
	v_med3_f32 v93, v66, s60, v115
	v_pk_mul_f32 v[64:65], v[92:93], v[64:65] op_sel_hi:[0,1]
	v_med3_f32 v94, v67, s60, v115
	s_waitcnt vmcnt(14)
	v_pk_mul_f32 v[64:65], v[64:65], v[26:27]
	v_cvt_pk_fp8_f32 v96, v93, v94 op_sel:[0,0,1]
	v_pk_mul_f32 v[70:71], v[92:93], v[70:71] op_sel_hi:[0,1]
	v_med3_f32 v93, v64, s60, v115
	v_med3_f32 v94, v65, s60, v115
	v_cvt_pk_fp8_f32 v97, v93, v94
	v_pk_mul_f32 v[70:71], v[70:71], v[28:29]
	v_mov_b32_e32 v98, 0
	v_med3_f32 v93, v70, s60, v115
	v_pk_mul_f32 v[68:69], v[92:93], v[68:69] op_sel_hi:[0,1]
	v_med3_f32 v94, v71, s60, v115
	s_waitcnt vmcnt(13)
	v_pk_mul_f32 v[68:69], v[68:69], v[30:31]
	v_cvt_pk_fp8_f32 v97, v93, v94 op_sel:[0,0,1]
	v_pk_mul_f32 v[72:73], v[92:93], v[72:73] op_sel_hi:[0,1]
	v_med3_f32 v92, v68, s60, v115
	v_med3_f32 v93, v69, s60, v115
	v_cvt_pk_fp8_f32 v98, v92, v93
	v_pk_mul_f32 v[72:73], v[72:73], v[32:33]
	s_nop 0
	v_med3_f32 v92, v72, s60, v115
	v_med3_f32 v93, v73, s60, v115
	v_cvt_pk_fp8_f32 v98, v92, v93 op_sel:[0,0,1]
	ds_read_b128 v[150:153], v34 offset:0
	ds_read_b128 v[154:157], v34 offset:1024
	ds_read_b128 v[158:161], v34 offset:2048
	ds_read_b128 v[162:165], v34 offset:3072
	ds_read_b128 v[166:169], v34 offset:4096
	ds_read_b128 v[170:173], v34 offset:5120
	ds_read_b128 v[174:177], v34 offset:6144
	global_store_dword v[74:75], v96, off offset:1280
	global_store_dword v[74:75], v97, off offset:1536
	global_store_dword v[74:75], v98, off offset:1792
	ds_read_b128 v[178:181], v34 offset:7168
	s_waitcnt lgkmcnt(7)
	v_mul_f32_e32 v93, v151, v43
	v_fmac_f32_e32 v93, v150, v42
	v_mul_f32_e32 v92, v153, v47
	v_fmac_f32_e32 v92, v152, v46
	v_add_f32_e32 v92, v93, v92
	v_add_f32_e32 v100, 0, v92
	ds_read_b128 v[150:153], v34 offset:8192
	s_waitcnt lgkmcnt(7)
	v_mul_f32_e32 v97, v155, v45
	v_fmac_f32_e32 v97, v154, v44
	v_mul_f32_e32 v96, v157, v51
	v_fmac_f32_e32 v96, v156, v50
	v_add_f32_e32 v96, v97, v96
	v_add_f32_e32 v100, v100, v96
	ds_read_b128 v[154:157], v34 offset:9216
	s_waitcnt lgkmcnt(7)
	v_mul_f32_e32 v93, v159, v49
	v_fmac_f32_e32 v93, v158, v48
	v_mul_f32_e32 v92, v161, v55
	v_fmac_f32_e32 v92, v160, v54
	v_add_f32_e32 v92, v93, v92
	v_add_f32_e32 v100, v100, v92
	ds_read_b128 v[158:161], v34 offset:10240
	s_waitcnt lgkmcnt(7)
	v_mul_f32_e32 v97, v163, v53
	v_fmac_f32_e32 v97, v162, v52
	v_mul_f32_e32 v96, v165, v59
	v_fmac_f32_e32 v96, v164, v58
	v_add_f32_e32 v96, v97, v96
	v_add_f32_e32 v100, v100, v96
	ds_read_b128 v[162:165], v34 offset:11264
	s_waitcnt lgkmcnt(7)
	v_mul_f32_e32 v93, v167, v57
	v_fmac_f32_e32 v93, v166, v56
	v_mul_f32_e32 v92, v169, v63
	v_fmac_f32_e32 v92, v168, v62
	v_add_f32_e32 v92, v93, v92
	v_add_f32_e32 v100, v100, v92
	ds_read_b128 v[166:169], v34 offset:12288
	s_waitcnt lgkmcnt(7)
	v_mul_f32_e32 v97, v171, v61
	v_fmac_f32_e32 v97, v170, v60
	v_mul_f32_e32 v96, v173, v67
	v_fmac_f32_e32 v96, v172, v66
	v_add_f32_e32 v96, v97, v96
	v_add_f32_e32 v100, v100, v96
	ds_read_b128 v[170:173], v34 offset:13312
	s_waitcnt lgkmcnt(7)
	v_mul_f32_e32 v93, v175, v65
	v_fmac_f32_e32 v93, v174, v64
	v_mul_f32_e32 v92, v177, v71
	v_fmac_f32_e32 v92, v176, v70
	v_add_f32_e32 v92, v93, v92
	s_waitcnt lgkmcnt(6)
	v_mul_f32_e32 v93, v179, v69
	v_mul_f32_e32 v94, v181, v73
	v_fmac_f32_e32 v93, v178, v68
	v_fmac_f32_e32 v94, v180, v72
	v_add_f32_e32 v92, v100, v92
	v_add_f32_e32 v93, v93, v94
	v_add_f32_e32 v92, v92, v93
	s_nop 1
	v_add_f32_dpp v92, v92, v92 quad_perm:[1,0,3,2] row_mask:0xf bank_mask:0xf bound_ctrl:1
	s_nop 1
	v_add_f32_dpp v92, v92, v92 quad_perm:[2,3,0,1] row_mask:0xf bank_mask:0xf bound_ctrl:1
	s_nop 1
	v_add_f32_dpp v92, v92, v92 row_half_mirror row_mask:0xf bank_mask:0xf bound_ctrl:1
	s_nop 1
	v_add_f32_dpp v96, v92, v92 row_mirror row_mask:0xf bank_mask:0xf bound_ctrl:1
	ds_read_b128 v[174:177], v34 offset:14336
	v_readlane_b32 s0, v96, 0
	v_readlane_b32 s39, v96, 16
	v_readlane_b32 s1, v96, 32
	v_readlane_b32 s52, v96, 48
	ds_read_b128 v[178:181], v34 offset:15360
	s_waitcnt lgkmcnt(7)
	v_mul_f32_e32 v93, v151, v43
	v_fmac_f32_e32 v93, v150, v42
	v_mul_f32_e32 v92, v153, v47
	v_fmac_f32_e32 v92, v152, v46
	v_add_f32_e32 v92, v93, v92
	s_waitcnt lgkmcnt(6)
	v_mul_f32_e32 v97, v155, v45
	v_add_f32_e32 v100, 0, v92
	v_fmac_f32_e32 v97, v154, v44
	v_mul_f32_e32 v96, v157, v51
	ds_read_b128 v[150:153], v34 offset:16384
	v_fmac_f32_e32 v96, v156, v50
	v_add_f32_e32 v96, v97, v96
	v_add_f32_e32 v100, v100, v96
	ds_read_b128 v[154:157], v34 offset:17408
	s_waitcnt lgkmcnt(7)
	v_mul_f32_e32 v93, v159, v49
	v_fmac_f32_e32 v93, v158, v48
	v_mul_f32_e32 v92, v161, v55
	v_fmac_f32_e32 v92, v160, v54
	v_add_f32_e32 v92, v93, v92
	s_waitcnt lgkmcnt(6)
	v_mul_f32_e32 v97, v163, v53
	v_add_f32_e32 v100, v100, v92
	v_fmac_f32_e32 v97, v162, v52
	v_mul_f32_e32 v96, v165, v59
	ds_read_b128 v[158:161], v34 offset:18432
	v_fmac_f32_e32 v96, v164, v58
	v_add_f32_e32 v96, v97, v96
	v_add_f32_e32 v100, v100, v96
	ds_read_b128 v[162:165], v34 offset:19456
	s_waitcnt lgkmcnt(7)
	v_mul_f32_e32 v93, v167, v57
	v_fmac_f32_e32 v93, v166, v56
	v_mul_f32_e32 v92, v169, v63
	v_fmac_f32_e32 v92, v168, v62
	v_add_f32_e32 v92, v93, v92
	s_waitcnt lgkmcnt(6)
	v_mul_f32_e32 v97, v171, v61
	v_add_f32_e32 v100, v100, v92
	v_fmac_f32_e32 v97, v170, v60
	v_mul_f32_e32 v96, v173, v67
	ds_read_b128 v[166:169], v34 offset:20480
	v_fmac_f32_e32 v96, v172, v66
	v_add_f32_e32 v96, v97, v96
	v_add_f32_e32 v100, v100, v96
	ds_read_b128 v[170:173], v34 offset:21504
	s_waitcnt lgkmcnt(7)
	v_mul_f32_e32 v93, v175, v65
	v_fmac_f32_e32 v93, v174, v64
	v_mul_f32_e32 v92, v177, v71
	v_fmac_f32_e32 v92, v176, v70
	v_add_f32_e32 v92, v93, v92
	s_waitcnt lgkmcnt(6)
	v_mul_f32_e32 v93, v179, v69
	v_mul_f32_e32 v94, v181, v73
	v_fmac_f32_e32 v93, v178, v68
	v_fmac_f32_e32 v94, v180, v72
	v_add_f32_e32 v92, v100, v92
	v_add_f32_e32 v93, v93, v94
	v_add_f32_e32 v92, v92, v93
	s_nop 1
	v_add_f32_dpp v92, v92, v92 quad_perm:[1,0,3,2] row_mask:0xf bank_mask:0xf bound_ctrl:1
	s_nop 1
	v_add_f32_dpp v92, v92, v92 quad_perm:[2,3,0,1] row_mask:0xf bank_mask:0xf bound_ctrl:1
	s_nop 1
	v_add_f32_dpp v92, v92, v92 row_half_mirror row_mask:0xf bank_mask:0xf bound_ctrl:1
	s_nop 1
	v_add_f32_dpp v96, v92, v92 row_mirror row_mask:0xf bank_mask:0xf bound_ctrl:1
	ds_read_b128 v[174:177], v34 offset:22528
	v_readlane_b32 s6, v96, 0
	v_readlane_b32 s53, v96, 16
	v_readlane_b32 s7, v96, 32
	v_readlane_b32 s63, v96, 48
	ds_read_b128 v[178:181], v34 offset:23552
	s_waitcnt lgkmcnt(7)
	v_mul_f32_e32 v93, v151, v43
	v_fmac_f32_e32 v93, v150, v42
	v_mul_f32_e32 v92, v153, v47
	v_fmac_f32_e32 v92, v152, v46
	v_add_f32_e32 v92, v93, v92
	s_waitcnt lgkmcnt(6)
	v_mul_f32_e32 v97, v155, v45
	v_add_f32_e32 v100, 0, v92
	v_fmac_f32_e32 v97, v154, v44
	v_mul_f32_e32 v96, v157, v51
	ds_read_b128 v[150:153], v34 offset:24576
	v_fmac_f32_e32 v96, v156, v50
	v_add_f32_e32 v96, v97, v96
	v_add_f32_e32 v100, v100, v96
	ds_read_b128 v[154:157], v34 offset:25600
	s_waitcnt lgkmcnt(7)
	v_mul_f32_e32 v93, v159, v49
	v_fmac_f32_e32 v93, v158, v48
	v_mul_f32_e32 v92, v161, v55
	v_fmac_f32_e32 v92, v160, v54
	v_add_f32_e32 v92, v93, v92
	s_waitcnt lgkmcnt(6)
	v_mul_f32_e32 v97, v163, v53
	v_add_f32_e32 v100, v100, v92
	v_fmac_f32_e32 v97, v162, v52
	v_mul_f32_e32 v96, v165, v59
	ds_read_b128 v[158:161], v34 offset:26624
	v_fmac_f32_e32 v96, v164, v58
	v_add_f32_e32 v96, v97, v96
	v_add_f32_e32 v100, v100, v96
	ds_read_b128 v[162:165], v34 offset:27648
	s_waitcnt lgkmcnt(7)
	v_mul_f32_e32 v93, v167, v57
	v_fmac_f32_e32 v93, v166, v56
	v_mul_f32_e32 v92, v169, v63
	v_fmac_f32_e32 v92, v168, v62
	v_add_f32_e32 v92, v93, v92
	s_waitcnt lgkmcnt(6)
	v_mul_f32_e32 v97, v171, v61
	v_add_f32_e32 v100, v100, v92
	v_fmac_f32_e32 v97, v170, v60
	v_mul_f32_e32 v96, v173, v67
	ds_read_b128 v[166:169], v34 offset:28672
	v_fmac_f32_e32 v96, v172, v66
	v_add_f32_e32 v96, v97, v96
	v_add_f32_e32 v100, v100, v96
	ds_read_b128 v[170:173], v34 offset:29696
	s_waitcnt lgkmcnt(7)
	v_mul_f32_e32 v93, v175, v65
	v_fmac_f32_e32 v93, v174, v64
	v_mul_f32_e32 v92, v177, v71
	v_fmac_f32_e32 v92, v176, v70
	v_add_f32_e32 v92, v93, v92
	s_waitcnt lgkmcnt(6)
	v_mul_f32_e32 v93, v179, v69
	v_mul_f32_e32 v94, v181, v73
	v_fmac_f32_e32 v93, v178, v68
	v_fmac_f32_e32 v94, v180, v72
	v_add_f32_e32 v92, v100, v92
	v_add_f32_e32 v93, v93, v94
	v_add_f32_e32 v92, v92, v93
	s_nop 1
	v_add_f32_dpp v92, v92, v92 quad_perm:[1,0,3,2] row_mask:0xf bank_mask:0xf bound_ctrl:1
	s_nop 1
	v_add_f32_dpp v92, v92, v92 quad_perm:[2,3,0,1] row_mask:0xf bank_mask:0xf bound_ctrl:1
	s_nop 1
	v_add_f32_dpp v92, v92, v92 row_half_mirror row_mask:0xf bank_mask:0xf bound_ctrl:1
	s_nop 1
	v_add_f32_dpp v96, v92, v92 row_mirror row_mask:0xf bank_mask:0xf bound_ctrl:1
	ds_read_b128 v[174:177], v34 offset:30720
	v_readlane_b32 s8, v96, 0
	v_readlane_b32 s64, v96, 16
	v_readlane_b32 s9, v96, 32
	v_readlane_b32 s65, v96, 48
	ds_read_b128 v[178:181], v34 offset:31744
	s_waitcnt lgkmcnt(7)
	v_mul_f32_e32 v93, v151, v43
	v_fmac_f32_e32 v93, v150, v42
	v_mul_f32_e32 v92, v153, v47
	v_fmac_f32_e32 v92, v152, v46
	v_add_f32_e32 v92, v93, v92
	s_waitcnt lgkmcnt(6)
	v_mul_f32_e32 v97, v155, v45
	v_add_f32_e32 v100, 0, v92
	v_fmac_f32_e32 v97, v154, v44
	v_mul_f32_e32 v96, v157, v51
	ds_read_b128 v[150:153], v34 offset:32768
	v_fmac_f32_e32 v96, v156, v50
	v_add_f32_e32 v96, v97, v96
	v_add_f32_e32 v100, v100, v96
	ds_read_b128 v[154:157], v34 offset:33792
	s_waitcnt lgkmcnt(7)
	v_mul_f32_e32 v93, v159, v49
	v_fmac_f32_e32 v93, v158, v48
	v_mul_f32_e32 v92, v161, v55
	v_fmac_f32_e32 v92, v160, v54
	v_add_f32_e32 v92, v93, v92
	s_waitcnt lgkmcnt(6)
	v_mul_f32_e32 v97, v163, v53
	v_add_f32_e32 v100, v100, v92
	v_fmac_f32_e32 v97, v162, v52
	v_mul_f32_e32 v96, v165, v59
	ds_read_b128 v[158:161], v34 offset:34816
	v_fmac_f32_e32 v96, v164, v58
	v_add_f32_e32 v96, v97, v96
	v_add_f32_e32 v100, v100, v96
	ds_read_b128 v[162:165], v34 offset:35840
	s_waitcnt lgkmcnt(7)
	v_mul_f32_e32 v93, v167, v57
	v_fmac_f32_e32 v93, v166, v56
	v_mul_f32_e32 v92, v169, v63
	v_fmac_f32_e32 v92, v168, v62
	v_add_f32_e32 v92, v93, v92
	s_waitcnt lgkmcnt(6)
	v_mul_f32_e32 v97, v171, v61
	v_add_f32_e32 v100, v100, v92
	v_fmac_f32_e32 v97, v170, v60
	v_mul_f32_e32 v96, v173, v67
	ds_read_b128 v[166:169], v34 offset:36864
	v_fmac_f32_e32 v96, v172, v66
	v_add_f32_e32 v96, v97, v96
	v_add_f32_e32 v100, v100, v96
	ds_read_b128 v[170:173], v34 offset:37888
	s_waitcnt lgkmcnt(7)
	v_mul_f32_e32 v93, v175, v65
	v_fmac_f32_e32 v93, v174, v64
	v_mul_f32_e32 v92, v177, v71
	v_fmac_f32_e32 v92, v176, v70
	v_add_f32_e32 v92, v93, v92
	s_waitcnt lgkmcnt(6)
	v_mul_f32_e32 v93, v179, v69
	v_mul_f32_e32 v94, v181, v73
	v_fmac_f32_e32 v93, v178, v68
	v_fmac_f32_e32 v94, v180, v72
	v_add_f32_e32 v92, v100, v92
	v_add_f32_e32 v93, v93, v94
	v_add_f32_e32 v92, v92, v93
	s_nop 1
	v_add_f32_dpp v92, v92, v92 quad_perm:[1,0,3,2] row_mask:0xf bank_mask:0xf bound_ctrl:1
	s_nop 1
	v_add_f32_dpp v92, v92, v92 quad_perm:[2,3,0,1] row_mask:0xf bank_mask:0xf bound_ctrl:1
	s_nop 1
	v_add_f32_dpp v92, v92, v92 row_half_mirror row_mask:0xf bank_mask:0xf bound_ctrl:1
	s_nop 1
	v_add_f32_dpp v96, v92, v92 row_mirror row_mask:0xf bank_mask:0xf bound_ctrl:1
	ds_read_b128 v[174:177], v34 offset:38912
	v_readlane_b32 s14, v96, 0
	v_readlane_b32 s66, v96, 16
	v_readlane_b32 s15, v96, 32
	v_readlane_b32 s67, v96, 48
	ds_read_b128 v[178:181], v34 offset:39936
	s_waitcnt lgkmcnt(7)
	v_mul_f32_e32 v93, v151, v43
	v_fmac_f32_e32 v93, v150, v42
	v_mul_f32_e32 v92, v153, v47
	v_fmac_f32_e32 v92, v152, v46
	v_add_f32_e32 v92, v93, v92
	s_waitcnt lgkmcnt(6)
	v_mul_f32_e32 v97, v155, v45
	v_add_f32_e32 v100, 0, v92
	v_fmac_f32_e32 v97, v154, v44
	v_mul_f32_e32 v96, v157, v51
	ds_read_b128 v[150:153], v34 offset:40960
	v_fmac_f32_e32 v96, v156, v50
	v_add_f32_e32 v96, v97, v96
	v_add_f32_e32 v100, v100, v96
	ds_read_b128 v[154:157], v34 offset:41984
	s_waitcnt lgkmcnt(7)
	v_mul_f32_e32 v93, v159, v49
	v_fmac_f32_e32 v93, v158, v48
	v_mul_f32_e32 v92, v161, v55
	v_fmac_f32_e32 v92, v160, v54
	v_add_f32_e32 v92, v93, v92
	s_waitcnt lgkmcnt(6)
	v_mul_f32_e32 v97, v163, v53
	v_add_f32_e32 v100, v100, v92
	v_fmac_f32_e32 v97, v162, v52
	v_mul_f32_e32 v96, v165, v59
	ds_read_b128 v[158:161], v34 offset:43008
	v_fmac_f32_e32 v96, v164, v58
	v_add_f32_e32 v96, v97, v96
	v_add_f32_e32 v100, v100, v96
	ds_read_b128 v[162:165], v34 offset:44032
	s_waitcnt lgkmcnt(7)
	v_mul_f32_e32 v93, v167, v57
	v_fmac_f32_e32 v93, v166, v56
	v_mul_f32_e32 v92, v169, v63
	v_fmac_f32_e32 v92, v168, v62
	v_add_f32_e32 v92, v93, v92
	s_waitcnt lgkmcnt(6)
	v_mul_f32_e32 v97, v171, v61
	v_add_f32_e32 v100, v100, v92
	v_fmac_f32_e32 v97, v170, v60
	v_mul_f32_e32 v96, v173, v67
	ds_read_b128 v[166:169], v34 offset:45056
	v_fmac_f32_e32 v96, v172, v66
	v_add_f32_e32 v96, v97, v96
	v_add_f32_e32 v100, v100, v96
	ds_read_b128 v[170:173], v34 offset:46080
	s_waitcnt lgkmcnt(7)
	v_mul_f32_e32 v93, v175, v65
	v_fmac_f32_e32 v93, v174, v64
	v_mul_f32_e32 v92, v177, v71
	v_fmac_f32_e32 v92, v176, v70
	v_add_f32_e32 v92, v93, v92
	s_waitcnt lgkmcnt(6)
	v_mul_f32_e32 v93, v179, v69
	v_mul_f32_e32 v94, v181, v73
	v_fmac_f32_e32 v93, v178, v68
	v_fmac_f32_e32 v94, v180, v72
	v_add_f32_e32 v92, v100, v92
	v_add_f32_e32 v93, v93, v94
	v_add_f32_e32 v92, v92, v93
	s_nop 1
	v_add_f32_dpp v92, v92, v92 quad_perm:[1,0,3,2] row_mask:0xf bank_mask:0xf bound_ctrl:1
	s_nop 1
	v_add_f32_dpp v92, v92, v92 quad_perm:[2,3,0,1] row_mask:0xf bank_mask:0xf bound_ctrl:1
	s_nop 1
	v_add_f32_dpp v92, v92, v92 row_half_mirror row_mask:0xf bank_mask:0xf bound_ctrl:1
	s_nop 1
	v_add_f32_dpp v96, v92, v92 row_mirror row_mask:0xf bank_mask:0xf bound_ctrl:1
	ds_read_b128 v[174:177], v34 offset:47104
	v_readlane_b32 s16, v96, 0
	v_readlane_b32 s69, v96, 16
	v_readlane_b32 s17, v96, 32
	v_readlane_b32 s70, v96, 48
	ds_read_b128 v[178:181], v34 offset:48128
	s_waitcnt lgkmcnt(7)
	v_mul_f32_e32 v93, v151, v43
	v_fmac_f32_e32 v93, v150, v42
	v_mul_f32_e32 v92, v153, v47
	v_fmac_f32_e32 v92, v152, v46
	v_add_f32_e32 v92, v93, v92
	s_waitcnt lgkmcnt(6)
	v_mul_f32_e32 v97, v155, v45
	v_add_f32_e32 v100, 0, v92
	v_fmac_f32_e32 v97, v154, v44
	v_mul_f32_e32 v96, v157, v51
	ds_read_b128 v[150:153], v34 offset:49152
	v_fmac_f32_e32 v96, v156, v50
	v_add_f32_e32 v96, v97, v96
	v_add_f32_e32 v100, v100, v96
	ds_read_b128 v[154:157], v34 offset:50176
	s_waitcnt lgkmcnt(7)
	v_mul_f32_e32 v93, v159, v49
	v_fmac_f32_e32 v93, v158, v48
	v_mul_f32_e32 v92, v161, v55
	v_fmac_f32_e32 v92, v160, v54
	v_add_f32_e32 v92, v93, v92
	s_waitcnt lgkmcnt(6)
	v_mul_f32_e32 v97, v163, v53
	v_add_f32_e32 v100, v100, v92
	v_fmac_f32_e32 v97, v162, v52
	v_mul_f32_e32 v96, v165, v59
	ds_read_b128 v[158:161], v34 offset:51200
	v_fmac_f32_e32 v96, v164, v58
	v_add_f32_e32 v96, v97, v96
	v_add_f32_e32 v100, v100, v96
	ds_read_b128 v[162:165], v34 offset:52224
	s_waitcnt lgkmcnt(7)
	v_mul_f32_e32 v93, v167, v57
	v_fmac_f32_e32 v93, v166, v56
	v_mul_f32_e32 v92, v169, v63
	v_fmac_f32_e32 v92, v168, v62
	v_add_f32_e32 v92, v93, v92
	s_waitcnt lgkmcnt(6)
	v_mul_f32_e32 v97, v171, v61
	v_add_f32_e32 v100, v100, v92
	v_fmac_f32_e32 v97, v170, v60
	v_mul_f32_e32 v96, v173, v67
	ds_read_b128 v[166:169], v34 offset:53248
	v_fmac_f32_e32 v96, v172, v66
	v_add_f32_e32 v96, v97, v96
	v_add_f32_e32 v100, v100, v96
	ds_read_b128 v[170:173], v34 offset:54272
	s_waitcnt lgkmcnt(7)
	v_mul_f32_e32 v93, v175, v65
	v_fmac_f32_e32 v93, v174, v64
	v_mul_f32_e32 v92, v177, v71
	v_fmac_f32_e32 v92, v176, v70
	v_add_f32_e32 v92, v93, v92
	s_waitcnt lgkmcnt(6)
	v_mul_f32_e32 v93, v179, v69
	v_mul_f32_e32 v94, v181, v73
	v_fmac_f32_e32 v93, v178, v68
	v_fmac_f32_e32 v94, v180, v72
	v_add_f32_e32 v92, v100, v92
	v_add_f32_e32 v93, v93, v94
	v_add_f32_e32 v92, v92, v93
	s_nop 1
	v_add_f32_dpp v92, v92, v92 quad_perm:[1,0,3,2] row_mask:0xf bank_mask:0xf bound_ctrl:1
	s_nop 1
	v_add_f32_dpp v92, v92, v92 quad_perm:[2,3,0,1] row_mask:0xf bank_mask:0xf bound_ctrl:1
	s_nop 1
	v_add_f32_dpp v92, v92, v92 row_half_mirror row_mask:0xf bank_mask:0xf bound_ctrl:1
	s_nop 1
	v_add_f32_dpp v96, v92, v92 row_mirror row_mask:0xf bank_mask:0xf bound_ctrl:1
	ds_read_b128 v[174:177], v34 offset:55296
	v_readlane_b32 s18, v96, 0
	v_readlane_b32 s71, v96, 16
	v_readlane_b32 s19, v96, 32
	v_readlane_b32 s72, v96, 48
	ds_read_b128 v[178:181], v34 offset:56320
	s_waitcnt lgkmcnt(7)
	v_mul_f32_e32 v93, v151, v43
	v_fmac_f32_e32 v93, v150, v42
	v_mul_f32_e32 v92, v153, v47
	v_fmac_f32_e32 v92, v152, v46
	v_add_f32_e32 v92, v93, v92
	s_waitcnt lgkmcnt(6)
	v_mul_f32_e32 v97, v155, v45
	v_add_f32_e32 v100, 0, v92
	v_fmac_f32_e32 v97, v154, v44
	v_mul_f32_e32 v96, v157, v51
	ds_read_b128 v[150:153], v34 offset:57344
	v_fmac_f32_e32 v96, v156, v50
	v_add_f32_e32 v96, v97, v96
	v_add_f32_e32 v100, v100, v96
	ds_read_b128 v[154:157], v34 offset:58368
	s_waitcnt lgkmcnt(7)
	v_mul_f32_e32 v93, v159, v49
	v_fmac_f32_e32 v93, v158, v48
	v_mul_f32_e32 v92, v161, v55
	v_fmac_f32_e32 v92, v160, v54
	v_add_f32_e32 v92, v93, v92
	s_waitcnt lgkmcnt(6)
	v_mul_f32_e32 v97, v163, v53
	v_add_f32_e32 v100, v100, v92
	v_fmac_f32_e32 v97, v162, v52
	v_mul_f32_e32 v96, v165, v59
	ds_read_b128 v[158:161], v34 offset:59392
	v_fmac_f32_e32 v96, v164, v58
	v_add_f32_e32 v96, v97, v96
	v_add_f32_e32 v100, v100, v96
	ds_read_b128 v[162:165], v34 offset:60416
	s_waitcnt lgkmcnt(7)
	v_mul_f32_e32 v93, v167, v57
	v_fmac_f32_e32 v93, v166, v56
	v_mul_f32_e32 v92, v169, v63
	v_fmac_f32_e32 v92, v168, v62
	v_add_f32_e32 v92, v93, v92
	s_waitcnt lgkmcnt(6)
	v_mul_f32_e32 v97, v171, v61
	v_add_f32_e32 v100, v100, v92
	v_fmac_f32_e32 v97, v170, v60
	v_mul_f32_e32 v96, v173, v67
	ds_read_b128 v[166:169], v34 offset:61440
	v_fmac_f32_e32 v96, v172, v66
	v_add_f32_e32 v96, v97, v96
	v_add_f32_e32 v100, v100, v96
	ds_read_b128 v[170:173], v34 offset:62464
	s_waitcnt lgkmcnt(7)
	v_mul_f32_e32 v93, v175, v65
	v_fmac_f32_e32 v93, v174, v64
	v_mul_f32_e32 v92, v177, v71
	v_fmac_f32_e32 v92, v176, v70
	v_add_f32_e32 v92, v93, v92
	s_waitcnt lgkmcnt(6)
	v_mul_f32_e32 v93, v179, v69
	v_mul_f32_e32 v94, v181, v73
	v_fmac_f32_e32 v93, v178, v68
	v_fmac_f32_e32 v94, v180, v72
	v_add_f32_e32 v92, v100, v92
	v_add_f32_e32 v93, v93, v94
	v_add_f32_e32 v92, v92, v93
	s_nop 1
	v_add_f32_dpp v92, v92, v92 quad_perm:[1,0,3,2] row_mask:0xf bank_mask:0xf bound_ctrl:1
	s_nop 1
	v_add_f32_dpp v92, v92, v92 quad_perm:[2,3,0,1] row_mask:0xf bank_mask:0xf bound_ctrl:1
	s_nop 1
	v_add_f32_dpp v92, v92, v92 row_half_mirror row_mask:0xf bank_mask:0xf bound_ctrl:1
	s_nop 1
	v_add_f32_dpp v96, v92, v92 row_mirror row_mask:0xf bank_mask:0xf bound_ctrl:1
	ds_read_b128 v[174:177], v34 offset:63488
	v_readlane_b32 s20, v96, 0
	v_readlane_b32 s73, v96, 16
	v_readlane_b32 s21, v96, 32
	v_readlane_b32 s74, v96, 48
	ds_read_b128 v[178:181], v34 offset:64512
	s_waitcnt lgkmcnt(7)
	v_mul_f32_e32 v93, v151, v43
	v_fmac_f32_e32 v93, v150, v42
	v_mul_f32_e32 v92, v153, v47
	v_fmac_f32_e32 v92, v152, v46
	v_add_f32_e32 v92, v93, v92
	s_waitcnt lgkmcnt(6)
	v_mul_f32_e32 v97, v155, v45
	v_add_f32_e32 v100, 0, v92
	v_fmac_f32_e32 v97, v154, v44
	v_mul_f32_e32 v96, v157, v51
	v_fmac_f32_e32 v96, v156, v50
	v_add_f32_e32 v96, v97, v96
	v_add_f32_e32 v100, v100, v96
	s_waitcnt lgkmcnt(5)
	v_mul_f32_e32 v93, v159, v49
	v_fmac_f32_e32 v93, v158, v48
	v_mul_f32_e32 v92, v161, v55
	v_fmac_f32_e32 v92, v160, v54
	v_add_f32_e32 v92, v93, v92
	s_waitcnt lgkmcnt(4)
	v_mul_f32_e32 v97, v163, v53
	v_add_f32_e32 v100, v100, v92
	v_fmac_f32_e32 v97, v162, v52
	v_mul_f32_e32 v96, v165, v59
	v_fmac_f32_e32 v96, v164, v58
	v_add_f32_e32 v96, v97, v96
	v_add_f32_e32 v100, v100, v96
	s_waitcnt lgkmcnt(3)
	v_mul_f32_e32 v93, v167, v57
	v_fmac_f32_e32 v93, v166, v56
	v_mul_f32_e32 v92, v169, v63
	v_fmac_f32_e32 v92, v168, v62
	v_add_f32_e32 v92, v93, v92
	s_waitcnt lgkmcnt(2)
	v_mul_f32_e32 v97, v171, v61
	v_add_f32_e32 v100, v100, v92
	v_fmac_f32_e32 v97, v170, v60
	v_mul_f32_e32 v96, v173, v67
	v_fmac_f32_e32 v96, v172, v66
	v_add_f32_e32 v96, v97, v96
	v_add_f32_e32 v100, v100, v96
	s_waitcnt lgkmcnt(1)
	v_mul_f32_e32 v93, v175, v65
	v_fmac_f32_e32 v93, v174, v64
	v_mul_f32_e32 v92, v177, v71
	v_fmac_f32_e32 v92, v176, v70
	v_add_f32_e32 v92, v93, v92
	s_waitcnt lgkmcnt(0)
	v_mul_f32_e32 v93, v179, v69
	v_mul_f32_e32 v94, v181, v73
	v_fmac_f32_e32 v93, v178, v68
	v_fmac_f32_e32 v94, v180, v72
	v_add_f32_e32 v92, v100, v92
	v_add_f32_e32 v93, v93, v94
	v_add_f32_e32 v92, v92, v93
	s_nop 1
	v_add_f32_dpp v92, v92, v92 quad_perm:[1,0,3,2] row_mask:0xf bank_mask:0xf bound_ctrl:1
	s_nop 1
	v_add_f32_dpp v92, v92, v92 quad_perm:[2,3,0,1] row_mask:0xf bank_mask:0xf bound_ctrl:1
	s_nop 1
	v_add_f32_dpp v92, v92, v92 row_half_mirror row_mask:0xf bank_mask:0xf bound_ctrl:1
	s_nop 1
	v_add_f32_dpp v92, v92, v92 row_mirror row_mask:0xf bank_mask:0xf bound_ctrl:1
	s_nop 0
	v_readlane_b32 s50, v92, 0
	v_readlane_b32 s75, v92, 16
	v_readlane_b32 s51, v92, 32
	v_readlane_b32 s76, v92, 48
	s_and_saveexec_b64 s[46:47], s[4:5]
	s_cbranch_execz .LBB0_1381
	v_readlane_b32 s80, v251, 0
	v_readlane_b32 s82, v251, 2
	v_readlane_b32 s83, v251, 3
	s_nop 4
	global_load_dwordx4 v[92:95], v35, s[82:83] offset:16
	global_load_dwordx4 v[96:99], v35, s[82:83]
	v_mov_b32_e32 v100, s75
	v_mov_b32_e32 v101, s76
	v_mov_b32_e32 v120, s53
	v_mov_b32_e32 v121, s63
	v_mov_b32_e32 v122, s39
	v_mov_b32_e32 v123, s52
	v_mov_b32_e32 v102, s73
	v_mov_b32_e32 v103, s74
	v_mov_b32_e32 v104, s71
	v_mov_b32_e32 v105, s72
	v_mov_b32_e32 v106, s69
	v_mov_b32_e32 v107, s70
	v_pk_add_f32 v[100:101], s[50:51], v[100:101]
	v_pk_add_f32 v[120:121], s[6:7], v[120:121]
	v_pk_add_f32 v[122:123], s[0:1], v[122:123]
	v_pk_add_f32 v[102:103], s[20:21], v[102:103]
	v_pk_add_f32 v[104:105], s[18:19], v[104:105]
	v_pk_add_f32 v[106:107], s[16:17], v[106:107]
	v_add_f32_e32 v117, v100, v101
	v_mov_b32_e32 v100, v122
	v_mov_b32_e32 v101, v120
	v_mov_b32_e32 v120, v123
	v_mov_b32_e32 v118, s64
	v_mov_b32_e32 v119, s65
	v_add_f32_e32 v102, v102, v103
	v_add_f32_e32 v103, v104, v105
	v_add_f32_e32 v104, v106, v107
	v_pk_add_f32 v[100:101], v[100:101], v[120:121]
	v_pk_add_f32 v[118:119], s[8:9], v[118:119]
	v_mov_b32_e32 v108, s66
	v_mov_b32_e32 v109, s67
	v_add_f32_e32 v106, v118, v119
	v_pk_add_f32 v[108:109], s[14:15], v[108:109]
	s_mov_b64 s[48:49], exec
	v_add_f32_e32 v105, v108, v109
	v_readlane_b32 s81, v251, 1
	v_readlane_b32 s84, v251, 4
	v_readlane_b32 s85, v251, 5
	v_readlane_b32 s86, v251, 6
	v_readlane_b32 s87, v251, 7
	s_waitcnt vmcnt(1)
	v_add_f32_e32 v94, v94, v102
	v_add_f32_e32 v102, v93, v103
	v_add_f32_e32 v103, v92, v104
	s_waitcnt vmcnt(0)
	v_pk_add_f32 v[92:93], v[96:97], v[100:101]
	v_add_f32_e32 v98, v98, v106
	v_cmp_gt_f32_e32 vcc, v93, v92
	v_add_f32_e32 v99, v99, v105
	v_add_f32_e32 v95, v95, v117
	v_cndmask_b32_e32 v96, v92, v93, vcc
	v_cmp_gt_f32_e64 s[6:7], v98, v96
	v_cndmask_b32_e64 v97, 0, 1, vcc
	v_cmp_nlt_f32_e64 s[0:1], s62, v92
	v_cndmask_b32_e64 v96, v96, v98, s[6:7]
	v_cmp_gt_f32_e32 vcc, v99, v96
	v_readfirstlane_b32 s39, v97
	s_nop 0
	v_cndmask_b32_e32 v96, v96, v99, vcc
	v_cmp_gt_f32_e64 s[8:9], v103, v96
	s_nop 1
	v_cndmask_b32_e64 v96, v96, v103, s[8:9]
	v_cmp_gt_f32_e64 s[14:15], v102, v96
	s_nop 1
	v_cndmask_b32_e64 v96, v96, v102, s[14:15]
	v_cmp_gt_f32_e64 s[16:17], v94, v96
	s_nop 1
	v_cndmask_b32_e64 v96, v96, v94, s[16:17]
	v_cmp_ngt_f32_e64 s[18:19], v95, v96
	s_and_b64 s[20:21], s[18:19], s[16:17]
	s_and_b64 s[6:7], s[6:7], exec
	s_cselect_b32 s39, 2, s39
	s_and_b64 s[6:7], vcc, exec
	s_cselect_b32 s39, 3, s39
	s_and_b64 s[6:7], s[8:9], exec
	s_cselect_b32 s8, 4, s39
	s_and_b64 s[6:7], s[14:15], exec
	s_cselect_b32 s8, 5, s8
	s_and_b64 s[6:7], s[16:17], exec
	s_cselect_b32 s8, 6, s8
	s_and_b64 s[6:7], s[18:19], exec
	s_cselect_b32 s39, s8, 7
	s_cmp_lg_u32 s39, 5
	s_cselect_b64 s[16:17], -1, 0
	s_cmp_lg_u32 s39, 4
	s_cselect_b64 s[14:15], -1, 0
	s_cmp_lg_u32 s39, 3
	s_cselect_b64 s[8:9], -1, 0
	s_cmp_lg_u32 s39, 2
	s_cselect_b64 s[6:7], -1, 0
	s_cmp_lg_u32 s39, 1
	s_cselect_b64 s[50:51], -1, 0
	s_cmp_eq_u32 s39, 0
	s_cselect_b64 s[52:53], -1, 0
	s_or_b64 vcc, s[52:53], s[0:1]
	v_cndmask_b32_e32 v92, v92, v116, vcc
	v_cmp_gt_f32_e64 s[0:1], v93, v92
	v_cndmask_b32_e64 v97, 0, -1, vcc
	s_and_b64 vcc, s[50:51], s[0:1]
	v_cndmask_b32_e32 v92, v92, v93, vcc
	v_cmp_gt_f32_e64 s[0:1], v98, v92
	s_and_b64 s[0:1], s[6:7], s[0:1]
	v_cndmask_b32_e64 v96, v95, v96, s[18:19]
	v_cndmask_b32_e64 v92, v92, v98, s[0:1]
	v_cmp_gt_f32_e64 s[6:7], v99, v92
	s_and_b64 s[6:7], s[8:9], s[6:7]
	v_readfirstlane_b32 s50, v97
	v_cndmask_b32_e64 v92, v92, v99, s[6:7]
	v_cmp_gt_f32_e64 s[8:9], v103, v92
	s_and_b64 s[8:9], s[14:15], s[8:9]
	s_nop 0
	v_cndmask_b32_e64 v92, v92, v103, s[8:9]
	v_cmp_gt_f32_e64 s[14:15], v102, v92
	s_and_b64 s[14:15], s[16:17], s[14:15]
	s_nop 0
	v_cndmask_b32_e64 v92, v92, v102, s[14:15]
	v_cmp_ngt_f32_e64 s[16:17], v94, v92
	s_or_b64 s[16:17], s[20:21], s[16:17]
	s_nop 0
	v_cndmask_b32_e64 v92, v94, v92, s[16:17]
	v_cmp_gt_f32_e64 s[20:21], v95, v92
	s_and_b64 s[18:19], s[18:19], s[20:21]
	v_cndmask_b32_e64 v92, v92, v95, s[18:19]
	v_sub_f32_e32 v92, v92, v96
	v_mul_f32_e32 v92, 0x3fb8aa3b, v92
	v_exp_f32_e32 v92, v92
	s_and_b64 s[20:21], vcc, exec
	s_cselect_b32 s20, 1, s50
	s_and_b64 s[0:1], s[0:1], exec
	v_add_f32_e32 v92, 1.0, v92
	v_div_scale_f32 v93, s[0:1], v92, v92, 1.0
	v_rcp_f32_e32 v94, v93
	s_cselect_b32 s20, 2, s20
	s_and_b64 s[0:1], s[6:7], exec
	s_cselect_b32 s6, 3, s20
	s_and_b64 s[0:1], s[8:9], exec
	s_cselect_b32 s6, 4, s6
	s_and_b64 s[0:1], s[14:15], exec
	s_cselect_b32 s6, 5, s6
	s_and_b64 s[0:1], s[16:17], exec
	v_fma_f32 v95, -v93, v94, 1.0
	s_cselect_b32 s6, s6, 6
	s_and_b64 s[0:1], s[18:19], exec
	v_fmac_f32_e32 v94, v95, v94
	v_div_scale_f32 v95, vcc, 1.0, v92, 1.0
	s_cselect_b32 s6, 7, s6
	v_mul_f32_e32 v96, v95, v94
	v_fma_f32 v97, -v93, v96, v95
	s_lshl_b32 s0, s6, 8
	v_fmac_f32_e32 v96, v97, v94
	s_add_i32 s7, s0, s39
	v_fma_f32 v93, -v93, v96, v95
	s_add_u32 s0, s56, s28
	v_div_fmas_f32 v93, v93, v94, v96
	s_addc_u32 s1, s57, s29
	v_mov_b32_e32 v94, s7
	v_div_fixup_f32 v92, v93, v92, 1.0
	global_store_dword v113, v94, s[0:1]
	s_add_u32 s0, s56, s42
	v_sub_f32_e32 v93, 1.0, v92
	s_addc_u32 s1, s57, s43
	global_store_dwordx2 v114, v[92:93], s[0:1]
	v_mbcnt_lo_u32_b32 v92, s48, 0
	v_mbcnt_hi_u32_b32 v92, s49, v92
	v_cmp_eq_u32_e32 vcc, 0, v92
	s_and_saveexec_b64 s[0:1], vcc
	s_cbranch_execz .LBB0_1379
	s_lshl_b32 s7, s39, 2
	s_add_i32 s7, s7, 0
	s_add_i32 s7, s7, 0x10000
	s_bcnt1_i32_b64 s8, s[48:49]
	v_mov_b32_e32 v92, s7
	v_mov_b32_e32 v93, s8
	ds_add_u32 v92, v93

.LBB0_1383:
	s_waitcnt vmcnt(15)
	v_lshlrev_b32_e32 v92, 16, v90
	v_and_b32_e32 v93, 0xffff0000, v90
	v_lshlrev_b32_e32 v90, 16, v91
	v_and_b32_e32 v91, 0xffff0000, v91
	s_waitcnt vmcnt(14)
	v_lshlrev_b32_e32 v95, 16, v89
	v_lshlrev_b32_e32 v94, 16, v88
	v_and_b32_e32 v89, 0xffff0000, v89
	v_and_b32_e32 v88, 0xffff0000, v88
	s_waitcnt vmcnt(12)
	v_lshlrev_b32_e32 v119, 16, v80
	v_and_b32_e32 v121, 0xffff0000, v80
	s_waitcnt vmcnt(8)
	v_lshlrev_b32_e32 v109, 16, v76
	v_and_b32_e32 v107, 0xffff0000, v76
	v_mul_f32_e32 v76, v91, v91
	v_mul_f32_e32 v80, v93, v93
	v_lshlrev_b32_e32 v122, 16, v81
	v_and_b32_e32 v123, 0xffff0000, v81
	v_lshlrev_b32_e32 v96, 16, v78
	v_and_b32_e32 v97, 0xffff0000, v78
	v_lshlrev_b32_e32 v102, 16, v79
	v_and_b32_e32 v103, 0xffff0000, v79
	v_lshlrev_b32_e32 v104, 16, v77
	v_and_b32_e32 v105, 0xffff0000, v77
	v_pk_fma_f32 v[76:77], v[90:91], v[90:91], v[76:77] op_sel_hi:[1,1,0]
	v_pk_mul_f32 v[78:79], v[88:89], v[88:89]
	v_pk_fma_f32 v[80:81], v[92:93], v[92:93], v[80:81] op_sel_hi:[1,1,0]
	v_lshlrev_b32_e32 v98, 16, v82
	v_and_b32_e32 v99, 0xffff0000, v82
	v_lshlrev_b32_e32 v100, 16, v83
	v_and_b32_e32 v101, 0xffff0000, v83
	v_pk_fma_f32 v[78:79], v[94:95], v[94:95], v[78:79]
	v_mov_b32_e32 v118, v80
	v_mov_b32_e32 v82, v76
	v_mov_b32_e32 v83, v119
	v_lshlrev_b32_e32 v128, 16, v84
	v_and_b32_e32 v130, 0xffff0000, v84
	v_mul_f32_e32 v84, v121, v121
	v_pk_add_f32 v[76:77], v[80:81], v[76:77]
	v_pk_mul_f32 v[80:81], v[118:119], v[82:83]
	v_pk_add_f32 v[78:79], v[78:79], v[78:79] op_sel:[0,1] op_sel_hi:[1,0]
	v_mov_b32_e32 v77, v81
	v_mov_b32_e32 v79, v84
	v_pk_add_f32 v[76:77], v[76:77], v[78:79]
	v_mul_f32_e32 v78, v99, v99
	v_mul_f32_e32 v80, v101, v101
	v_lshlrev_b32_e32 v124, 16, v86
	v_and_b32_e32 v126, 0xffff0000, v86
	v_lshlrev_b32_e32 v129, 16, v85
	v_and_b32_e32 v131, 0xffff0000, v85
	v_mul_f32_e32 v85, v122, v122
	v_mul_f32_e32 v86, v123, v123
	v_pk_fma_f32 v[78:79], v[98:99], v[98:99], v[78:79] op_sel_hi:[1,1,0]
	v_pk_fma_f32 v[80:81], v[100:101], v[100:101], v[80:81] op_sel_hi:[1,1,0]
	v_mov_b32_e32 v79, v85
	v_mov_b32_e32 v81, v86
	v_and_b32_e32 v127, 0xffff0000, v87
	v_pk_add_f32 v[78:79], v[78:79], v[80:81]
	v_lshlrev_b32_e32 v125, 16, v87
	v_pk_add_f32 v[76:77], v[76:77], v[78:79]
	v_pk_mul_f32 v[78:79], v[126:127], v[126:127]
	v_pk_add_f32 v[76:77], v[76:77], v[76:77] op_sel:[0,1] op_sel_hi:[1,0]
	v_pk_fma_f32 v[78:79], v[124:125], v[124:125], v[78:79]
	v_pk_mul_f32 v[80:81], v[130:131], v[130:131]
	v_pk_add_f32 v[78:79], v[78:79], v[78:79] op_sel:[0,1] op_sel_hi:[1,0]
	v_mov_b32_e32 v108, v76
	v_mov_b32_e32 v82, v78
	v_mov_b32_e32 v83, v109
	v_pk_fma_f32 v[80:81], v[128:129], v[128:129], v[80:81]
	v_pk_add_f32 v[76:77], v[76:77], v[78:79]
	v_pk_mul_f32 v[78:79], v[108:109], v[82:83]
	v_mul_f32_e32 v84, v107, v107
	v_mov_b32_e32 v77, v79
	v_pk_add_f32 v[78:79], v[80:81], v[80:81] op_sel:[0,1] op_sel_hi:[1,0]
	v_mul_f32_e32 v80, v103, v103
	v_mov_b32_e32 v79, v84
	v_pk_add_f32 v[76:77], v[76:77], v[78:79]
	v_mul_f32_e32 v78, v97, v97
	v_mul_f32_e32 v85, v104, v104
	v_mul_f32_e32 v86, v105, v105
	v_pk_fma_f32 v[78:79], v[96:97], v[96:97], v[78:79] op_sel_hi:[1,1,0]
	v_pk_fma_f32 v[80:81], v[102:103], v[102:103], v[80:81] op_sel_hi:[1,1,0]
	v_mov_b32_e32 v79, v85
	v_mov_b32_e32 v81, v86
	v_pk_add_f32 v[78:79], v[78:79], v[80:81]
	v_mov_b32_e32 v82, 0
	v_pk_add_f32 v[76:77], v[76:77], v[78:79]
	v_mov_b32_e32 v106, 0
	v_add_f32_e32 v76, v76, v77
	v_mov_b32_e32 v120, v119
	v_mov_b32_e32 v117, 0
	v_add_f32_dpp v76, v76, v76 quad_perm:[1,0,3,2] row_mask:0xf bank_mask:0xf bound_ctrl:1
	s_nop 1
	v_add_f32_dpp v76, v76, v76 quad_perm:[2,3,0,1] row_mask:0xf bank_mask:0xf bound_ctrl:1
	s_nop 1
	v_add_f32_dpp v76, v76, v76 row_half_mirror row_mask:0xf bank_mask:0xf bound_ctrl:1
	s_nop 1
	v_add_f32_dpp v76, v76, v76 row_mirror row_mask:0xf bank_mask:0xf bound_ctrl:1
	s_nop 0
	v_readlane_b32 s6, v76, 16
	v_readlane_b32 s7, v76, 48
	v_readlane_b32 s0, v76, 0
	v_readlane_b32 s1, v76, 32
	v_mov_b32_e32 v76, s6
	v_mov_b32_e32 v77, s7
	v_pk_add_f32 v[76:77], s[0:1], v[76:77]
	s_nop 0
	v_add_f32_e32 v76, v76, v77
	v_fmamk_f32 v76, v76, 0x3a000000, v111
	v_mul_f32_e32 v77, 0x4f800000, v76
	v_cmp_gt_f32_e32 vcc, s35, v76
	s_nop 1
	v_cndmask_b32_e32 v76, v76, v77, vcc
	v_sqrt_f32_e32 v77, v76
	s_nop 0
	v_add_u32_e32 v78, -1, v77
	v_fma_f32 v79, -v78, v77, v76
	v_cmp_ge_f32_e64 s[0:1], 0, v79
	v_add_u32_e32 v79, 1, v77
	s_nop 0
	v_cndmask_b32_e64 v78, v77, v78, s[0:1]
	v_fma_f32 v77, -v79, v77, v76
	v_cmp_lt_f32_e64 s[0:1], 0, v77
	s_nop 1
	v_cndmask_b32_e64 v77, v78, v79, s[0:1]
	v_mul_f32_e32 v78, 0x37800000, v77
	v_cndmask_b32_e32 v77, v77, v78, vcc
	v_cmp_class_f32_e32 vcc, v76, v112
	s_nop 1
	v_cndmask_b32_e32 v76, v77, v76, vcc
	v_div_scale_f32 v77, s[0:1], v76, v76, 1.0
	v_rcp_f32_e32 v78, v77
	s_nop 0
	v_fma_f32 v79, -v77, v78, 1.0
	v_fmac_f32_e32 v78, v79, v78
	v_div_scale_f32 v79, vcc, 1.0, v76, 1.0
	v_mul_f32_e32 v80, v79, v78
	v_fma_f32 v81, -v77, v80, v79
	v_fmac_f32_e32 v80, v81, v78
	v_fma_f32 v77, -v77, v80, v79
	v_div_fmas_f32 v77, v77, v78, v80
	v_div_fixup_f32 v108, v77, v76, 1.0
	v_pk_mul_f32 v[76:77], v[108:109], v[92:93] op_sel_hi:[0,1]
	v_pk_mul_f32 v[76:77], v[76:77], v[14:15]
	v_pk_mul_f32 v[78:79], v[108:109], v[90:91] op_sel_hi:[0,1]
	v_med3_f32 v80, v76, s60, v115
	v_med3_f32 v81, v77, s60, v115
	v_cvt_pk_fp8_f32 v82, v80, v81
	v_pk_mul_f32 v[78:79], v[78:79], v[16:17]
	v_pk_mul_f32 v[86:87], v[108:109], v[100:101] op_sel_hi:[0,1]
	v_med3_f32 v80, v78, s60, v115
	v_med3_f32 v81, v79, s60, v115
	v_cvt_pk_fp8_f32 v82, v80, v81 op_sel:[0,0,1]
	v_mov_b32_e32 v80, v94
	v_mov_b32_e32 v81, v88
	v_pk_mul_f32 v[80:81], v[108:109], v[80:81] op_sel_hi:[0,1]
	v_pk_mul_f32 v[84:85], v[80:81], v[2:3]
	v_mov_b32_e32 v88, v95
	v_med3_f32 v80, v84, s60, v115
	v_med3_f32 v81, v85, s60, v115
	v_cvt_pk_fp8_f32 v106, v80, v81
	global_store_dword v[74:75], v82, off offset:2048
	v_pk_mul_f32 v[82:83], v[108:109], v[88:89] op_sel_hi:[0,1]
	v_pk_mul_f32 v[82:83], v[82:83], v[4:5]
	v_pk_mul_f32 v[86:87], v[86:87], v[8:9]
	v_med3_f32 v80, v82, s60, v115
	v_med3_f32 v81, v83, s60, v115
	v_cvt_pk_fp8_f32 v106, v80, v81 op_sel:[0,0,1]
	v_pk_mul_f32 v[80:81], v[108:109], v[98:99] op_sel_hi:[0,1]
	v_pk_mul_f32 v[80:81], v[80:81], v[6:7]
	v_mov_b32_e32 v98, 0
	v_med3_f32 v88, v80, s60, v115
	v_med3_f32 v89, v81, s60, v115
	v_cvt_pk_fp8_f32 v98, v88, v89
	v_med3_f32 v88, v86, s60, v115
	v_med3_f32 v89, v87, s60, v115
	v_mov_b32_e32 v99, 0
	v_cvt_pk_fp8_f32 v98, v88, v89 op_sel:[0,0,1]
	v_pk_mul_f32 v[88:89], v[108:109], v[120:121] op_sel_hi:[0,1]
	v_pk_mul_f32 v[90:91], v[88:89], v[10:11]
	v_pk_mul_f32 v[92:93], v[108:109], v[122:123] op_sel_hi:[0,1]
	v_med3_f32 v88, v90, s60, v115
	v_med3_f32 v89, v91, s60, v115
	v_cvt_pk_fp8_f32 v99, v88, v89
	v_pk_mul_f32 v[88:89], v[92:93], v[12:13]
	v_pk_mul_f32 v[96:97], v[108:109], v[96:97] op_sel_hi:[0,1]
	v_med3_f32 v92, v88, s60, v115
	v_med3_f32 v93, v89, s60, v115
	v_cvt_pk_fp8_f32 v99, v92, v93 op_sel:[0,0,1]
	v_mov_b32_e32 v92, v124
	v_mov_b32_e32 v93, v126
	v_pk_mul_f32 v[92:93], v[108:109], v[92:93] op_sel_hi:[0,1]
	v_pk_mul_f32 v[92:93], v[92:93], v[18:19]
	v_mov_b32_e32 v126, v125
	v_med3_f32 v100, v92, s60, v115
	v_med3_f32 v101, v93, s60, v115
	v_cvt_pk_fp8_f32 v117, v100, v101
	v_pk_mul_f32 v[94:95], v[108:109], v[126:127] op_sel_hi:[0,1]
	v_pk_mul_f32 v[94:95], v[94:95], v[20:21]
	v_pk_mul_f32 v[96:97], v[96:97], v[26:27]
	v_med3_f32 v100, v94, s60, v115
	v_med3_f32 v101, v95, s60, v115
	v_cvt_pk_fp8_f32 v117, v100, v101 op_sel:[0,0,1]
	global_store_dword v[74:75], v106, off offset:2304
	global_store_dword v[74:75], v98, off offset:2560
	global_store_dword v[74:75], v99, off offset:2816
	global_store_dword v[74:75], v117, off offset:3072
	v_mov_b32_e32 v98, v128
	v_mov_b32_e32 v99, v130
	v_pk_mul_f32 v[98:99], v[108:109], v[98:99] op_sel_hi:[0,1]
	v_pk_mul_f32 v[100:101], v[98:99], v[22:23]
	v_mov_b32_e32 v117, 0
	v_med3_f32 v98, v100, s60, v115
	v_med3_f32 v99, v101, s60, v115
	v_mov_b32_e32 v130, v129
	v_cvt_pk_fp8_f32 v117, v98, v99
	v_pk_mul_f32 v[118:119], v[108:109], v[130:131] op_sel_hi:[0,1]
	v_pk_mul_f32 v[98:99], v[118:119], v[24:25]
	v_mov_b32_e32 v122, 0
	v_med3_f32 v106, v98, s60, v115
	v_med3_f32 v118, v99, s60, v115
	v_cvt_pk_fp8_f32 v117, v106, v118 op_sel:[0,0,1]
	v_med3_f32 v106, v96, s60, v115
	v_med3_f32 v118, v97, s60, v115
	v_cvt_pk_fp8_f32 v122, v106, v118
	v_pk_mul_f32 v[102:103], v[108:109], v[102:103] op_sel_hi:[0,1]
	v_pk_mul_f32 v[102:103], v[102:103], v[28:29]
	v_mov_b32_e32 v123, 0
	v_med3_f32 v106, v102, s60, v115
	v_med3_f32 v118, v103, s60, v115
	v_cvt_pk_fp8_f32 v122, v106, v118 op_sel:[0,0,1]
	v_mov_b32_e32 v106, v109
	v_pk_mul_f32 v[106:107], v[108:109], v[106:107] op_sel_hi:[0,1]
	v_pk_mul_f32 v[108:109], v[108:109], v[104:105] op_sel_hi:[0,1]
	v_pk_mul_f32 v[104:105], v[106:107], v[30:31]
	ds_read_b128 v[150:153], v34 offset:0
	ds_read_b128 v[154:157], v34 offset:1024
	ds_read_b128 v[158:161], v34 offset:2048
	ds_read_b128 v[162:165], v34 offset:3072
	ds_read_b128 v[166:169], v34 offset:4096
	ds_read_b128 v[170:173], v34 offset:5120
	ds_read_b128 v[174:177], v34 offset:6144
	v_med3_f32 v106, v104, s60, v115
	v_med3_f32 v107, v105, s60, v115
	v_cvt_pk_fp8_f32 v123, v106, v107
	v_pk_mul_f32 v[106:107], v[108:109], v[32:33]
	s_nop 0
	v_med3_f32 v108, v106, s60, v115
	v_med3_f32 v109, v107, s60, v115
	v_cvt_pk_fp8_f32 v123, v108, v109 op_sel:[0,0,1]
	global_store_dword v[74:75], v117, off offset:3328
	global_store_dword v[74:75], v122, off offset:3584
	global_store_dword v[74:75], v123, off offset:3840
	ds_read_b128 v[178:181], v34 offset:7168
	s_waitcnt lgkmcnt(7)
	v_mul_f32_e32 v74, v151, v77
	v_mul_f32_e32 v75, v153, v79
	v_fmac_f32_e32 v74, v150, v76
	v_fmac_f32_e32 v75, v152, v78
	ds_read_b128 v[150:153], v34 offset:8192
	v_add_f32_e32 v74, v74, v75
	s_waitcnt lgkmcnt(7)
	v_mul_f32_e32 v75, v155, v85
	v_mul_f32_e32 v108, v157, v83
	v_fmac_f32_e32 v75, v154, v84
	v_fmac_f32_e32 v108, v156, v82
	ds_read_b128 v[154:157], v34 offset:9216
	v_add_f32_e32 v74, 0, v74
	v_add_f32_e32 v75, v75, v108
	v_add_f32_e32 v74, v74, v75
	s_waitcnt lgkmcnt(7)
	v_mul_f32_e32 v75, v159, v81
	v_mul_f32_e32 v108, v161, v87
	v_fmac_f32_e32 v75, v158, v80
	v_fmac_f32_e32 v108, v160, v86
	ds_read_b128 v[158:161], v34 offset:10240
	v_add_f32_e32 v75, v75, v108
	v_add_f32_e32 v74, v74, v75
	s_waitcnt lgkmcnt(7)
	v_mul_f32_e32 v75, v163, v91
	v_mul_f32_e32 v108, v165, v89
	v_fmac_f32_e32 v75, v162, v90
	v_fmac_f32_e32 v108, v164, v88
	ds_read_b128 v[162:165], v34 offset:11264
	v_add_f32_e32 v75, v75, v108
	v_add_f32_e32 v74, v74, v75
	s_waitcnt lgkmcnt(7)
	v_mul_f32_e32 v75, v167, v93
	v_mul_f32_e32 v108, v169, v95
	v_fmac_f32_e32 v75, v166, v92
	v_fmac_f32_e32 v108, v168, v94
	ds_read_b128 v[166:169], v34 offset:12288
	v_add_f32_e32 v75, v75, v108
	v_add_f32_e32 v74, v74, v75
	s_waitcnt lgkmcnt(7)
	v_mul_f32_e32 v75, v171, v101
	v_mul_f32_e32 v108, v173, v99
	v_fmac_f32_e32 v75, v170, v100
	v_fmac_f32_e32 v108, v172, v98
	ds_read_b128 v[170:173], v34 offset:13312
	v_add_f32_e32 v75, v75, v108
	v_add_f32_e32 v74, v74, v75
	s_waitcnt lgkmcnt(7)
	v_mul_f32_e32 v75, v175, v97
	v_mul_f32_e32 v108, v177, v103
	v_fmac_f32_e32 v75, v174, v96
	v_fmac_f32_e32 v108, v176, v102
	v_add_f32_e32 v75, v75, v108
	v_add_f32_e32 v74, v74, v75
	ds_read_b128 v[174:177], v34 offset:14336
	s_waitcnt lgkmcnt(7)
	v_mul_f32_e32 v75, v179, v105
	v_mul_f32_e32 v108, v181, v107
	v_fmac_f32_e32 v75, v178, v104
	v_fmac_f32_e32 v108, v180, v106
	v_add_f32_e32 v75, v75, v108
	v_add_f32_e32 v74, v74, v75
	ds_read_b128 v[178:181], v34 offset:15360
	s_waitcnt lgkmcnt(7)
	v_mul_f32_e32 v75, v153, v79
	v_add_f32_dpp v74, v74, v74 quad_perm:[1,0,3,2] row_mask:0xf bank_mask:0xf bound_ctrl:1
	v_fmac_f32_e32 v75, v152, v78
	s_nop 0
	v_add_f32_dpp v74, v74, v74 quad_perm:[2,3,0,1] row_mask:0xf bank_mask:0xf bound_ctrl:1
	s_nop 1
	v_add_f32_dpp v74, v74, v74 row_half_mirror row_mask:0xf bank_mask:0xf bound_ctrl:1
	s_nop 1
	v_add_f32_dpp v74, v74, v74 row_mirror row_mask:0xf bank_mask:0xf bound_ctrl:1
	s_nop 0
	v_readlane_b32 s0, v74, 0
	v_readlane_b32 s39, v74, 16
	v_readlane_b32 s1, v74, 32
	v_readlane_b32 s63, v74, 48
	v_mul_f32_e32 v74, v151, v77
	v_fmac_f32_e32 v74, v150, v76
	ds_read_b128 v[150:153], v34 offset:16384
	v_add_f32_e32 v74, v74, v75
	s_waitcnt lgkmcnt(7)
	v_mul_f32_e32 v75, v155, v85
	v_mul_f32_e32 v108, v157, v83
	v_fmac_f32_e32 v75, v154, v84
	v_fmac_f32_e32 v108, v156, v82
	ds_read_b128 v[154:157], v34 offset:17408
	v_add_f32_e32 v74, 0, v74
	v_add_f32_e32 v75, v75, v108
	v_add_f32_e32 v74, v74, v75
	s_waitcnt lgkmcnt(7)
	v_mul_f32_e32 v75, v159, v81
	v_mul_f32_e32 v108, v161, v87
	v_fmac_f32_e32 v75, v158, v80
	v_fmac_f32_e32 v108, v160, v86
	ds_read_b128 v[158:161], v34 offset:18432
	v_add_f32_e32 v75, v75, v108
	v_add_f32_e32 v74, v74, v75
	s_waitcnt lgkmcnt(7)
	v_mul_f32_e32 v75, v163, v91
	v_mul_f32_e32 v108, v165, v89
	v_fmac_f32_e32 v75, v162, v90
	v_fmac_f32_e32 v108, v164, v88
	ds_read_b128 v[162:165], v34 offset:19456
	v_add_f32_e32 v75, v75, v108
	v_add_f32_e32 v74, v74, v75
	s_waitcnt lgkmcnt(7)
	v_mul_f32_e32 v75, v167, v93
	v_mul_f32_e32 v108, v169, v95
	v_fmac_f32_e32 v75, v166, v92
	v_fmac_f32_e32 v108, v168, v94
	ds_read_b128 v[166:169], v34 offset:20480
	v_add_f32_e32 v75, v75, v108
	v_add_f32_e32 v74, v74, v75
	s_waitcnt lgkmcnt(7)
	v_mul_f32_e32 v75, v171, v101
	v_mul_f32_e32 v108, v173, v99
	v_fmac_f32_e32 v75, v170, v100
	v_fmac_f32_e32 v108, v172, v98
	ds_read_b128 v[170:173], v34 offset:21504
	v_add_f32_e32 v75, v75, v108
	v_add_f32_e32 v74, v74, v75
	s_waitcnt lgkmcnt(7)
	v_mul_f32_e32 v75, v175, v97
	v_mul_f32_e32 v108, v177, v103
	v_fmac_f32_e32 v75, v174, v96
	v_fmac_f32_e32 v108, v176, v102
	v_add_f32_e32 v75, v75, v108
	v_add_f32_e32 v74, v74, v75
	ds_read_b128 v[174:177], v34 offset:22528
	s_waitcnt lgkmcnt(7)
	v_mul_f32_e32 v75, v179, v105
	v_mul_f32_e32 v108, v181, v107
	v_fmac_f32_e32 v75, v178, v104
	v_fmac_f32_e32 v108, v180, v106
	v_add_f32_e32 v75, v75, v108
	v_add_f32_e32 v74, v74, v75
	ds_read_b128 v[178:181], v34 offset:23552
	s_waitcnt lgkmcnt(7)
	v_mul_f32_e32 v75, v153, v79
	v_add_f32_dpp v74, v74, v74 quad_perm:[1,0,3,2] row_mask:0xf bank_mask:0xf bound_ctrl:1
	v_fmac_f32_e32 v75, v152, v78
	s_nop 0
	v_add_f32_dpp v74, v74, v74 quad_perm:[2,3,0,1] row_mask:0xf bank_mask:0xf bound_ctrl:1
	s_nop 1
	v_add_f32_dpp v74, v74, v74 row_half_mirror row_mask:0xf bank_mask:0xf bound_ctrl:1
	s_nop 1
	v_add_f32_dpp v74, v74, v74 row_mirror row_mask:0xf bank_mask:0xf bound_ctrl:1
	s_nop 0
	v_readlane_b32 s6, v74, 0
	v_readlane_b32 s64, v74, 16
	v_readlane_b32 s7, v74, 32
	v_readlane_b32 s65, v74, 48
	v_mul_f32_e32 v74, v151, v77
	v_fmac_f32_e32 v74, v150, v76
	ds_read_b128 v[150:153], v34 offset:24576
	v_add_f32_e32 v74, v74, v75
	s_waitcnt lgkmcnt(7)
	v_mul_f32_e32 v75, v155, v85
	v_mul_f32_e32 v108, v157, v83
	v_fmac_f32_e32 v75, v154, v84
	v_fmac_f32_e32 v108, v156, v82
	ds_read_b128 v[154:157], v34 offset:25600
	v_add_f32_e32 v74, 0, v74
	v_add_f32_e32 v75, v75, v108
	v_add_f32_e32 v74, v74, v75
	s_waitcnt lgkmcnt(7)
	v_mul_f32_e32 v75, v159, v81
	v_mul_f32_e32 v108, v161, v87
	v_fmac_f32_e32 v75, v158, v80
	v_fmac_f32_e32 v108, v160, v86
	ds_read_b128 v[158:161], v34 offset:26624
	v_add_f32_e32 v75, v75, v108
	v_add_f32_e32 v74, v74, v75
	s_waitcnt lgkmcnt(7)
	v_mul_f32_e32 v75, v163, v91
	v_mul_f32_e32 v108, v165, v89
	v_fmac_f32_e32 v75, v162, v90
	v_fmac_f32_e32 v108, v164, v88
	ds_read_b128 v[162:165], v34 offset:27648
	v_add_f32_e32 v75, v75, v108
	v_add_f32_e32 v74, v74, v75
	s_waitcnt lgkmcnt(7)
	v_mul_f32_e32 v75, v167, v93
	v_mul_f32_e32 v108, v169, v95
	v_fmac_f32_e32 v75, v166, v92
	v_fmac_f32_e32 v108, v168, v94
	ds_read_b128 v[166:169], v34 offset:28672
	v_add_f32_e32 v75, v75, v108
	v_add_f32_e32 v74, v74, v75
	s_waitcnt lgkmcnt(7)
	v_mul_f32_e32 v75, v171, v101
	v_mul_f32_e32 v108, v173, v99
	v_fmac_f32_e32 v75, v170, v100
	v_fmac_f32_e32 v108, v172, v98
	ds_read_b128 v[170:173], v34 offset:29696
	v_add_f32_e32 v75, v75, v108
	v_add_f32_e32 v74, v74, v75
	s_waitcnt lgkmcnt(7)
	v_mul_f32_e32 v75, v175, v97
	v_mul_f32_e32 v108, v177, v103
	v_fmac_f32_e32 v75, v174, v96
	v_fmac_f32_e32 v108, v176, v102
	v_add_f32_e32 v75, v75, v108
	v_add_f32_e32 v74, v74, v75
	ds_read_b128 v[174:177], v34 offset:30720
	s_waitcnt lgkmcnt(7)
	v_mul_f32_e32 v75, v179, v105
	v_mul_f32_e32 v108, v181, v107
	v_fmac_f32_e32 v75, v178, v104
	v_fmac_f32_e32 v108, v180, v106
	v_add_f32_e32 v75, v75, v108
	v_add_f32_e32 v74, v74, v75
	ds_read_b128 v[178:181], v34 offset:31744
	s_waitcnt lgkmcnt(7)
	v_mul_f32_e32 v75, v153, v79
	v_add_f32_dpp v74, v74, v74 quad_perm:[1,0,3,2] row_mask:0xf bank_mask:0xf bound_ctrl:1
	v_fmac_f32_e32 v75, v152, v78
	s_nop 0
	v_add_f32_dpp v74, v74, v74 quad_perm:[2,3,0,1] row_mask:0xf bank_mask:0xf bound_ctrl:1
	s_nop 1
	v_add_f32_dpp v74, v74, v74 row_half_mirror row_mask:0xf bank_mask:0xf bound_ctrl:1
	s_nop 1
	v_add_f32_dpp v74, v74, v74 row_mirror row_mask:0xf bank_mask:0xf bound_ctrl:1
	s_nop 0
	v_readlane_b32 s8, v74, 0
	v_readlane_b32 s66, v74, 16
	v_readlane_b32 s9, v74, 32
	v_readlane_b32 s67, v74, 48
	v_mul_f32_e32 v74, v151, v77
	v_fmac_f32_e32 v74, v150, v76
	ds_read_b128 v[150:153], v34 offset:32768
	v_add_f32_e32 v74, v74, v75
	s_waitcnt lgkmcnt(7)
	v_mul_f32_e32 v75, v155, v85
	v_mul_f32_e32 v108, v157, v83
	v_fmac_f32_e32 v75, v154, v84
	v_fmac_f32_e32 v108, v156, v82
	ds_read_b128 v[154:157], v34 offset:33792
	v_add_f32_e32 v74, 0, v74
	v_add_f32_e32 v75, v75, v108
	v_add_f32_e32 v74, v74, v75
	s_waitcnt lgkmcnt(7)
	v_mul_f32_e32 v75, v159, v81
	v_mul_f32_e32 v108, v161, v87
	v_fmac_f32_e32 v75, v158, v80
	v_fmac_f32_e32 v108, v160, v86
	ds_read_b128 v[158:161], v34 offset:34816
	v_add_f32_e32 v75, v75, v108
	v_add_f32_e32 v74, v74, v75
	s_waitcnt lgkmcnt(7)
	v_mul_f32_e32 v75, v163, v91
	v_mul_f32_e32 v108, v165, v89
	v_fmac_f32_e32 v75, v162, v90
	v_fmac_f32_e32 v108, v164, v88
	ds_read_b128 v[162:165], v34 offset:35840
	v_add_f32_e32 v75, v75, v108
	v_add_f32_e32 v74, v74, v75
	s_waitcnt lgkmcnt(7)
	v_mul_f32_e32 v75, v167, v93
	v_mul_f32_e32 v108, v169, v95
	v_fmac_f32_e32 v75, v166, v92
	v_fmac_f32_e32 v108, v168, v94
	ds_read_b128 v[166:169], v34 offset:36864
	v_add_f32_e32 v75, v75, v108
	v_add_f32_e32 v74, v74, v75
	s_waitcnt lgkmcnt(7)
	v_mul_f32_e32 v75, v171, v101
	v_mul_f32_e32 v108, v173, v99
	v_fmac_f32_e32 v75, v170, v100
	v_fmac_f32_e32 v108, v172, v98
	ds_read_b128 v[170:173], v34 offset:37888
	v_add_f32_e32 v75, v75, v108
	v_add_f32_e32 v74, v74, v75
	s_waitcnt lgkmcnt(7)
	v_mul_f32_e32 v75, v175, v97
	v_mul_f32_e32 v108, v177, v103
	v_fmac_f32_e32 v75, v174, v96
	v_fmac_f32_e32 v108, v176, v102
	v_add_f32_e32 v75, v75, v108
	v_add_f32_e32 v74, v74, v75
	s_waitcnt lgkmcnt(6)
	v_mul_f32_e32 v75, v179, v105
	v_mul_f32_e32 v108, v181, v107
	v_fmac_f32_e32 v75, v178, v104
	v_fmac_f32_e32 v108, v180, v106
	v_add_f32_e32 v75, v75, v108
	v_add_f32_e32 v74, v74, v75
	ds_read_b128 v[174:177], v34 offset:38912
	ds_read_b128 v[178:181], v34 offset:39936
	v_add_f32_dpp v74, v74, v74 quad_perm:[1,0,3,2] row_mask:0xf bank_mask:0xf bound_ctrl:1
	s_waitcnt lgkmcnt(7)
	v_mul_f32_e32 v75, v153, v79
	v_add_f32_dpp v74, v74, v74 quad_perm:[2,3,0,1] row_mask:0xf bank_mask:0xf bound_ctrl:1
	v_fmac_f32_e32 v75, v152, v78
	s_waitcnt lgkmcnt(6)
	v_mul_f32_e32 v108, v157, v83
	v_add_f32_dpp v74, v74, v74 row_half_mirror row_mask:0xf bank_mask:0xf bound_ctrl:1
	v_fmac_f32_e32 v108, v156, v82
	s_nop 0
	v_add_f32_dpp v74, v74, v74 row_mirror row_mask:0xf bank_mask:0xf bound_ctrl:1
	s_nop 0
	v_readlane_b32 s14, v74, 0
	v_readlane_b32 s69, v74, 16
	v_readlane_b32 s15, v74, 32
	v_readlane_b32 s70, v74, 48
	v_mul_f32_e32 v74, v151, v77
	v_fmac_f32_e32 v74, v150, v76
	ds_read_b128 v[150:153], v34 offset:40960
	v_add_f32_e32 v74, v74, v75
	v_mul_f32_e32 v75, v155, v85
	v_fmac_f32_e32 v75, v154, v84
	ds_read_b128 v[154:157], v34 offset:41984
	v_add_f32_e32 v74, 0, v74
	v_add_f32_e32 v75, v75, v108
	v_add_f32_e32 v74, v74, v75
	s_waitcnt lgkmcnt(7)
	v_mul_f32_e32 v75, v159, v81
	v_mul_f32_e32 v108, v161, v87
	v_fmac_f32_e32 v75, v158, v80
	v_fmac_f32_e32 v108, v160, v86
	ds_read_b128 v[158:161], v34 offset:43008
	v_add_f32_e32 v75, v75, v108
	v_add_f32_e32 v74, v74, v75
	s_waitcnt lgkmcnt(7)
	v_mul_f32_e32 v75, v163, v91
	v_mul_f32_e32 v108, v165, v89
	v_fmac_f32_e32 v75, v162, v90
	v_fmac_f32_e32 v108, v164, v88
	ds_read_b128 v[162:165], v34 offset:44032
	v_add_f32_e32 v75, v75, v108
	v_add_f32_e32 v74, v74, v75
	s_waitcnt lgkmcnt(7)
	v_mul_f32_e32 v75, v167, v93
	v_mul_f32_e32 v108, v169, v95
	v_fmac_f32_e32 v75, v166, v92
	v_fmac_f32_e32 v108, v168, v94
	ds_read_b128 v[166:169], v34 offset:45056
	v_add_f32_e32 v75, v75, v108
	v_add_f32_e32 v74, v74, v75
	s_waitcnt lgkmcnt(7)
	v_mul_f32_e32 v75, v171, v101
	v_mul_f32_e32 v108, v173, v99
	v_fmac_f32_e32 v75, v170, v100
	v_fmac_f32_e32 v108, v172, v98
	ds_read_b128 v[170:173], v34 offset:46080
	v_add_f32_e32 v75, v75, v108
	v_add_f32_e32 v74, v74, v75
	s_waitcnt lgkmcnt(7)
	v_mul_f32_e32 v75, v175, v97
	v_mul_f32_e32 v108, v177, v103
	v_fmac_f32_e32 v75, v174, v96
	v_fmac_f32_e32 v108, v176, v102
	v_add_f32_e32 v75, v75, v108
	v_add_f32_e32 v74, v74, v75
	s_waitcnt lgkmcnt(6)
	v_mul_f32_e32 v75, v179, v105
	v_mul_f32_e32 v108, v181, v107
	v_fmac_f32_e32 v75, v178, v104
	v_fmac_f32_e32 v108, v180, v106
	v_add_f32_e32 v75, v75, v108
	v_add_f32_e32 v74, v74, v75
	ds_read_b128 v[174:177], v34 offset:47104
	ds_read_b128 v[178:181], v34 offset:48128
	v_add_f32_dpp v74, v74, v74 quad_perm:[1,0,3,2] row_mask:0xf bank_mask:0xf bound_ctrl:1
	s_waitcnt lgkmcnt(7)
	v_mul_f32_e32 v75, v153, v79
	v_add_f32_dpp v74, v74, v74 quad_perm:[2,3,0,1] row_mask:0xf bank_mask:0xf bound_ctrl:1
	v_fmac_f32_e32 v75, v152, v78
	s_waitcnt lgkmcnt(6)
	v_mul_f32_e32 v108, v157, v83
	v_add_f32_dpp v74, v74, v74 row_half_mirror row_mask:0xf bank_mask:0xf bound_ctrl:1
	v_fmac_f32_e32 v108, v156, v82
	s_nop 0
	v_add_f32_dpp v74, v74, v74 row_mirror row_mask:0xf bank_mask:0xf bound_ctrl:1
	s_nop 0
	v_readlane_b32 s16, v74, 0
	v_readlane_b32 s71, v74, 16
	v_readlane_b32 s17, v74, 32
	v_readlane_b32 s72, v74, 48
	v_mul_f32_e32 v74, v151, v77
	v_fmac_f32_e32 v74, v150, v76
	ds_read_b128 v[150:153], v34 offset:49152
	v_add_f32_e32 v74, v74, v75
	v_mul_f32_e32 v75, v155, v85
	v_fmac_f32_e32 v75, v154, v84
	ds_read_b128 v[154:157], v34 offset:50176
	v_add_f32_e32 v74, 0, v74
	v_add_f32_e32 v75, v75, v108
	v_add_f32_e32 v74, v74, v75
	s_waitcnt lgkmcnt(7)
	v_mul_f32_e32 v75, v159, v81
	v_mul_f32_e32 v108, v161, v87
	v_fmac_f32_e32 v75, v158, v80
	v_fmac_f32_e32 v108, v160, v86
	ds_read_b128 v[158:161], v34 offset:51200
	v_add_f32_e32 v75, v75, v108
	v_add_f32_e32 v74, v74, v75
	s_waitcnt lgkmcnt(7)
	v_mul_f32_e32 v75, v163, v91
	v_mul_f32_e32 v108, v165, v89
	v_fmac_f32_e32 v75, v162, v90
	v_fmac_f32_e32 v108, v164, v88
	ds_read_b128 v[162:165], v34 offset:52224
	v_add_f32_e32 v75, v75, v108
	v_add_f32_e32 v74, v74, v75
	s_waitcnt lgkmcnt(7)
	v_mul_f32_e32 v75, v167, v93
	v_mul_f32_e32 v108, v169, v95
	v_fmac_f32_e32 v75, v166, v92
	v_fmac_f32_e32 v108, v168, v94
	ds_read_b128 v[166:169], v34 offset:53248
	v_add_f32_e32 v75, v75, v108
	v_add_f32_e32 v74, v74, v75
	s_waitcnt lgkmcnt(7)
	v_mul_f32_e32 v75, v171, v101
	v_mul_f32_e32 v108, v173, v99
	v_fmac_f32_e32 v75, v170, v100
	v_fmac_f32_e32 v108, v172, v98
	ds_read_b128 v[170:173], v34 offset:54272
	v_add_f32_e32 v75, v75, v108
	v_add_f32_e32 v74, v74, v75
	s_waitcnt lgkmcnt(7)
	v_mul_f32_e32 v75, v175, v97
	v_mul_f32_e32 v108, v177, v103
	v_fmac_f32_e32 v75, v174, v96
	v_fmac_f32_e32 v108, v176, v102
	v_add_f32_e32 v75, v75, v108
	v_add_f32_e32 v74, v74, v75
	s_waitcnt lgkmcnt(6)
	v_mul_f32_e32 v75, v179, v105
	v_mul_f32_e32 v108, v181, v107
	v_fmac_f32_e32 v75, v178, v104
	v_fmac_f32_e32 v108, v180, v106
	v_add_f32_e32 v75, v75, v108
	v_add_f32_e32 v74, v74, v75
	ds_read_b128 v[174:177], v34 offset:55296
	ds_read_b128 v[178:181], v34 offset:56320
	v_add_f32_dpp v74, v74, v74 quad_perm:[1,0,3,2] row_mask:0xf bank_mask:0xf bound_ctrl:1
	s_waitcnt lgkmcnt(7)
	v_mul_f32_e32 v75, v153, v79
	v_add_f32_dpp v74, v74, v74 quad_perm:[2,3,0,1] row_mask:0xf bank_mask:0xf bound_ctrl:1
	v_fmac_f32_e32 v75, v152, v78
	s_waitcnt lgkmcnt(6)
	v_mul_f32_e32 v108, v157, v83
	v_add_f32_dpp v74, v74, v74 row_half_mirror row_mask:0xf bank_mask:0xf bound_ctrl:1
	v_fmac_f32_e32 v108, v156, v82
	s_nop 0
	v_add_f32_dpp v74, v74, v74 row_mirror row_mask:0xf bank_mask:0xf bound_ctrl:1
	s_nop 0
	v_readlane_b32 s18, v74, 0
	v_readlane_b32 s73, v74, 16
	v_readlane_b32 s19, v74, 32
	v_readlane_b32 s74, v74, 48
	v_mul_f32_e32 v74, v151, v77
	v_fmac_f32_e32 v74, v150, v76
	ds_read_b128 v[150:153], v34 offset:57344
	v_add_f32_e32 v74, v74, v75
	v_mul_f32_e32 v75, v155, v85
	v_fmac_f32_e32 v75, v154, v84
	ds_read_b128 v[154:157], v34 offset:58368
	v_add_f32_e32 v74, 0, v74
	v_add_f32_e32 v75, v75, v108
	v_add_f32_e32 v74, v74, v75
	s_waitcnt lgkmcnt(7)
	v_mul_f32_e32 v75, v159, v81
	v_mul_f32_e32 v108, v161, v87
	v_fmac_f32_e32 v75, v158, v80
	v_fmac_f32_e32 v108, v160, v86
	ds_read_b128 v[158:161], v34 offset:59392
	v_add_f32_e32 v75, v75, v108
	v_add_f32_e32 v74, v74, v75
	s_waitcnt lgkmcnt(7)
	v_mul_f32_e32 v75, v163, v91
	v_mul_f32_e32 v108, v165, v89
	v_fmac_f32_e32 v75, v162, v90
	v_fmac_f32_e32 v108, v164, v88
	ds_read_b128 v[162:165], v34 offset:60416
	v_add_f32_e32 v75, v75, v108
	v_add_f32_e32 v74, v74, v75
	s_waitcnt lgkmcnt(7)
	v_mul_f32_e32 v75, v167, v93
	v_mul_f32_e32 v108, v169, v95
	v_fmac_f32_e32 v75, v166, v92
	v_fmac_f32_e32 v108, v168, v94
	ds_read_b128 v[166:169], v34 offset:61440
	v_add_f32_e32 v75, v75, v108
	v_add_f32_e32 v74, v74, v75
	s_waitcnt lgkmcnt(7)
	v_mul_f32_e32 v75, v171, v101
	v_mul_f32_e32 v108, v173, v99
	v_fmac_f32_e32 v75, v170, v100
	v_fmac_f32_e32 v108, v172, v98
	ds_read_b128 v[170:173], v34 offset:62464
	v_add_f32_e32 v75, v75, v108
	v_add_f32_e32 v74, v74, v75
	s_waitcnt lgkmcnt(7)
	v_mul_f32_e32 v75, v175, v97
	v_mul_f32_e32 v108, v177, v103
	v_fmac_f32_e32 v75, v174, v96
	v_fmac_f32_e32 v108, v176, v102
	v_add_f32_e32 v75, v75, v108
	v_add_f32_e32 v74, v74, v75
	s_waitcnt lgkmcnt(6)
	v_mul_f32_e32 v75, v179, v105
	v_mul_f32_e32 v108, v181, v107
	v_fmac_f32_e32 v75, v178, v104
	v_fmac_f32_e32 v108, v180, v106
	v_add_f32_e32 v75, v75, v108
	v_add_f32_e32 v74, v74, v75
	ds_read_b128 v[174:177], v34 offset:63488
	ds_read_b128 v[178:181], v34 offset:64512
	v_add_f32_dpp v74, v74, v74 quad_perm:[1,0,3,2] row_mask:0xf bank_mask:0xf bound_ctrl:1
	s_waitcnt lgkmcnt(7)
	v_mul_f32_e32 v75, v153, v79
	v_add_f32_dpp v74, v74, v74 quad_perm:[2,3,0,1] row_mask:0xf bank_mask:0xf bound_ctrl:1
	v_fmac_f32_e32 v75, v152, v78
	s_waitcnt lgkmcnt(6)
	v_mul_f32_e32 v79, v155, v85
	v_add_f32_dpp v74, v74, v74 row_half_mirror row_mask:0xf bank_mask:0xf bound_ctrl:1
	v_mul_f32_e32 v83, v157, v83
	v_fmac_f32_e32 v79, v154, v84
	v_add_f32_dpp v74, v74, v74 row_mirror row_mask:0xf bank_mask:0xf bound_ctrl:1
	v_fmac_f32_e32 v83, v156, v82
	v_readlane_b32 s20, v74, 0
	v_readlane_b32 s75, v74, 16
	v_readlane_b32 s21, v74, 32
	v_readlane_b32 s76, v74, 48
	v_mul_f32_e32 v74, v151, v77
	v_fmac_f32_e32 v74, v150, v76
	v_add_f32_e32 v74, v74, v75
	v_add_f32_e32 v78, 0, v74
	v_add_f32_e32 v79, v79, v83
	v_add_f32_e32 v78, v78, v79
	s_waitcnt lgkmcnt(5)
	v_mul_f32_e32 v75, v159, v81
	v_fmac_f32_e32 v75, v158, v80
	v_mul_f32_e32 v74, v161, v87
	v_fmac_f32_e32 v74, v160, v86
	v_add_f32_e32 v74, v75, v74
	v_add_f32_e32 v78, v78, v74
	s_waitcnt lgkmcnt(4)
	v_mul_f32_e32 v79, v163, v91
	v_mul_f32_e32 v80, v165, v89
	v_fmac_f32_e32 v79, v162, v90
	v_fmac_f32_e32 v80, v164, v88
	v_add_f32_e32 v79, v79, v80
	v_add_f32_e32 v82, v78, v79
	s_waitcnt lgkmcnt(3)
	v_mul_f32_e32 v75, v167, v93
	v_fmac_f32_e32 v75, v166, v92
	v_mul_f32_e32 v74, v169, v95
	v_fmac_f32_e32 v74, v168, v94
	v_add_f32_e32 v74, v75, v74
	s_waitcnt lgkmcnt(2)
	v_mul_f32_e32 v79, v171, v101
	v_add_f32_e32 v82, v82, v74
	v_fmac_f32_e32 v79, v170, v100
	v_mul_f32_e32 v78, v173, v99
	v_fmac_f32_e32 v78, v172, v98
	v_add_f32_e32 v78, v79, v78
	v_add_f32_e32 v82, v82, v78
	s_waitcnt lgkmcnt(1)
	v_mul_f32_e32 v75, v175, v97
	v_fmac_f32_e32 v75, v174, v96
	v_mul_f32_e32 v74, v177, v103
	v_fmac_f32_e32 v74, v176, v102
	v_add_f32_e32 v74, v75, v74
	s_waitcnt lgkmcnt(0)
	v_mul_f32_e32 v75, v179, v105
	v_mul_f32_e32 v76, v181, v107
	v_fmac_f32_e32 v75, v178, v104
	v_fmac_f32_e32 v76, v180, v106
	v_add_f32_e32 v74, v82, v74
	v_add_f32_e32 v75, v75, v76
	v_add_f32_e32 v74, v74, v75
	s_nop 1
	v_add_f32_dpp v74, v74, v74 quad_perm:[1,0,3,2] row_mask:0xf bank_mask:0xf bound_ctrl:1
	s_nop 1
	v_add_f32_dpp v74, v74, v74 quad_perm:[2,3,0,1] row_mask:0xf bank_mask:0xf bound_ctrl:1
	s_nop 1
	v_add_f32_dpp v74, v74, v74 row_half_mirror row_mask:0xf bank_mask:0xf bound_ctrl:1
	s_nop 1
	v_add_f32_dpp v74, v74, v74 row_mirror row_mask:0xf bank_mask:0xf bound_ctrl:1
	s_nop 0
	v_readlane_b32 s52, v74, 0
	v_readlane_b32 s77, v74, 16
	v_readlane_b32 s53, v74, 32
	v_readlane_b32 s78, v74, 48
	s_and_saveexec_b64 s[48:49], s[4:5]
	s_cbranch_execz .LBB0_1375
	v_readlane_b32 s80, v251, 0
	v_readlane_b32 s82, v251, 2
	v_readlane_b32 s83, v251, 3
	s_nop 4
	global_load_dwordx4 v[74:77], v35, s[82:83] offset:16
	global_load_dwordx4 v[78:81], v35, s[82:83]
	v_mov_b32_e32 v82, s77
	v_mov_b32_e32 v83, s78
	v_mov_b32_e32 v94, s64
	v_mov_b32_e32 v95, s65
	v_mov_b32_e32 v96, s39
	v_mov_b32_e32 v97, s63
	v_mov_b32_e32 v84, s75
	v_mov_b32_e32 v85, s76
	v_mov_b32_e32 v86, s73
	v_mov_b32_e32 v87, s74
	v_mov_b32_e32 v88, s71
	v_mov_b32_e32 v89, s72
	v_pk_add_f32 v[82:83], s[52:53], v[82:83]
	v_pk_add_f32 v[94:95], s[6:7], v[94:95]
	v_pk_add_f32 v[96:97], s[0:1], v[96:97]
	v_pk_add_f32 v[84:85], s[20:21], v[84:85]
	v_pk_add_f32 v[86:87], s[18:19], v[86:87]
	v_pk_add_f32 v[88:89], s[16:17], v[88:89]
	v_add_f32_e32 v98, v82, v83
	v_mov_b32_e32 v82, v96
	v_mov_b32_e32 v83, v94
	v_mov_b32_e32 v94, v97
	v_mov_b32_e32 v92, s66
	v_mov_b32_e32 v93, s67
	v_add_f32_e32 v84, v84, v85
	v_add_f32_e32 v85, v86, v87
	v_add_f32_e32 v86, v88, v89
	v_pk_add_f32 v[82:83], v[82:83], v[94:95]
	v_pk_add_f32 v[92:93], s[8:9], v[92:93]
	v_mov_b32_e32 v90, s69
	v_mov_b32_e32 v91, s70
	v_add_f32_e32 v88, v92, v93
	v_pk_add_f32 v[90:91], s[14:15], v[90:91]
	s_mov_b64 s[50:51], exec
	v_add_f32_e32 v87, v90, v91
	v_readlane_b32 s81, v251, 1
	v_readlane_b32 s84, v251, 4
	v_readlane_b32 s85, v251, 5
	v_readlane_b32 s86, v251, 6
	v_readlane_b32 s87, v251, 7
	s_waitcnt vmcnt(1)
	v_add_f32_e32 v76, v76, v84
	v_add_f32_e32 v84, v75, v85
	v_add_f32_e32 v85, v74, v86
	s_waitcnt vmcnt(0)
	v_pk_add_f32 v[74:75], v[78:79], v[82:83]
	v_add_f32_e32 v80, v80, v88
	v_cmp_gt_f32_e32 vcc, v75, v74
	v_add_f32_e32 v81, v81, v87
	v_add_f32_e32 v77, v77, v98
	v_cndmask_b32_e32 v78, v74, v75, vcc
	v_cmp_gt_f32_e64 s[6:7], v80, v78
	v_cndmask_b32_e64 v79, 0, 1, vcc
	v_cmp_nlt_f32_e64 s[0:1], s62, v74
	v_cndmask_b32_e64 v78, v78, v80, s[6:7]
	v_cmp_gt_f32_e32 vcc, v81, v78
	v_readfirstlane_b32 s39, v79
	s_nop 0
	v_cndmask_b32_e32 v78, v78, v81, vcc
	v_cmp_gt_f32_e64 s[8:9], v85, v78
	s_nop 1
	v_cndmask_b32_e64 v78, v78, v85, s[8:9]
	v_cmp_gt_f32_e64 s[14:15], v84, v78
	s_nop 1
	v_cndmask_b32_e64 v78, v78, v84, s[14:15]
	v_cmp_gt_f32_e64 s[16:17], v76, v78
	s_nop 1
	v_cndmask_b32_e64 v78, v78, v76, s[16:17]
	v_cmp_ngt_f32_e64 s[18:19], v77, v78
	s_and_b64 s[20:21], s[18:19], s[16:17]
	s_and_b64 s[6:7], s[6:7], exec
	s_cselect_b32 s39, 2, s39
	s_and_b64 s[6:7], vcc, exec
	s_cselect_b32 s39, 3, s39
	s_and_b64 s[6:7], s[8:9], exec
	s_cselect_b32 s8, 4, s39
	s_and_b64 s[6:7], s[14:15], exec
	s_cselect_b32 s8, 5, s8
	s_and_b64 s[6:7], s[16:17], exec
	s_cselect_b32 s8, 6, s8
	s_and_b64 s[6:7], s[18:19], exec
	s_cselect_b32 s52, s8, 7
	s_cmp_lg_u32 s52, 5
	s_cselect_b64 s[16:17], -1, 0
	s_cmp_lg_u32 s52, 4
	s_cselect_b64 s[14:15], -1, 0
	s_cmp_lg_u32 s52, 3
	s_cselect_b64 s[8:9], -1, 0
	s_cmp_lg_u32 s52, 2
	s_cselect_b64 s[6:7], -1, 0
	s_cmp_lg_u32 s52, 1
	s_cselect_b64 s[64:65], -1, 0
	s_cmp_eq_u32 s52, 0
	s_cselect_b64 s[66:67], -1, 0
	s_or_b64 vcc, s[66:67], s[0:1]
	v_cndmask_b32_e32 v74, v74, v116, vcc
	v_cmp_gt_f32_e64 s[0:1], v75, v74
	v_cndmask_b32_e64 v79, 0, -1, vcc
	s_and_b64 vcc, s[64:65], s[0:1]
	v_cndmask_b32_e32 v74, v74, v75, vcc
	v_cmp_gt_f32_e64 s[0:1], v80, v74
	s_and_b64 s[0:1], s[6:7], s[0:1]
	v_cndmask_b32_e64 v78, v77, v78, s[18:19]
	v_cndmask_b32_e64 v74, v74, v80, s[0:1]
	v_cmp_gt_f32_e64 s[6:7], v81, v74
	s_and_b64 s[6:7], s[8:9], s[6:7]
	v_readfirstlane_b32 s39, v79
	v_cndmask_b32_e64 v74, v74, v81, s[6:7]
	v_cmp_gt_f32_e64 s[8:9], v85, v74
	s_and_b64 s[8:9], s[14:15], s[8:9]
	s_nop 0
	v_cndmask_b32_e64 v74, v74, v85, s[8:9]
	v_cmp_gt_f32_e64 s[14:15], v84, v74
	s_and_b64 s[14:15], s[16:17], s[14:15]
	s_nop 0
	v_cndmask_b32_e64 v74, v74, v84, s[14:15]
	v_cmp_ngt_f32_e64 s[16:17], v76, v74
	s_or_b64 s[16:17], s[20:21], s[16:17]
	s_nop 0
	v_cndmask_b32_e64 v74, v76, v74, s[16:17]
	v_cmp_gt_f32_e64 s[20:21], v77, v74
	s_and_b64 s[18:19], s[18:19], s[20:21]
	v_cndmask_b32_e64 v74, v74, v77, s[18:19]
	v_sub_f32_e32 v74, v74, v78
	v_mul_f32_e32 v74, 0x3fb8aa3b, v74
	v_exp_f32_e32 v74, v74
	s_and_b64 s[20:21], vcc, exec
	s_cselect_b32 s20, 1, s39
	s_and_b64 s[0:1], s[0:1], exec
	v_add_f32_e32 v74, 1.0, v74
	v_div_scale_f32 v75, s[0:1], v74, v74, 1.0
	v_rcp_f32_e32 v76, v75
	s_cselect_b32 s20, 2, s20
	s_and_b64 s[0:1], s[6:7], exec
	s_cselect_b32 s6, 3, s20
	s_and_b64 s[0:1], s[8:9], exec
	s_cselect_b32 s6, 4, s6
	s_and_b64 s[0:1], s[14:15], exec
	s_cselect_b32 s6, 5, s6
	s_and_b64 s[0:1], s[16:17], exec
	v_fma_f32 v77, -v75, v76, 1.0
	s_cselect_b32 s6, s6, 6
	s_and_b64 s[0:1], s[18:19], exec
	v_fmac_f32_e32 v76, v77, v76
	v_div_scale_f32 v77, vcc, 1.0, v74, 1.0
	s_cselect_b32 s6, 7, s6
	v_mul_f32_e32 v78, v77, v76
	v_fma_f32 v79, -v75, v78, v77
	s_lshl_b32 s0, s6, 8
	v_fmac_f32_e32 v78, v79, v76
	s_add_i32 s7, s0, s52
	v_fma_f32 v75, -v75, v78, v77
	s_add_u32 s0, s56, s28
	v_div_fmas_f32 v75, v75, v76, v78
	s_addc_u32 s1, s57, s29
	v_mov_b32_e32 v76, s7
	s_ashr_i32 s39, s38, 31
	global_store_dword v113, v76, s[0:1] offset:4
	s_lshl_b64 s[0:1], s[38:39], 2
	v_div_fixup_f32 v74, v75, v74, 1.0
	s_add_u32 s0, s30, s0
	v_sub_f32_e32 v75, 1.0, v74
	s_addc_u32 s1, s31, s1
	global_store_dwordx2 v35, v[74:75], s[0:1]
	v_mbcnt_lo_u32_b32 v74, s50, 0
	v_mbcnt_hi_u32_b32 v74, s51, v74
	v_cmp_eq_u32_e32 vcc, 0, v74
	s_and_saveexec_b64 s[0:1], vcc
	s_cbranch_execz .LBB0_1386
	s_lshl_b32 s7, s52, 2
	s_add_i32 s7, s7, 0
	s_add_i32 s7, s7, 0x10000
	s_bcnt1_i32_b64 s8, s[50:51]
	v_mov_b32_e32 v74, s7
	v_mov_b32_e32 v75, s8
	ds_add_u32 v74, v75
